# v43 with s_setprio removed from the GEMM K-loops (A/B)
# speedup vs baseline: 1.0054x; 1.0054x over previous
.LBB0_177:
	s_add_u32 s28, s4, s26
	s_addc_u32 s29, s5, s27
	s_add_u32 s30, s28, 0xe000100
	s_addc_u32 s31, s29, 0
	ds_read_b128 v[24:27], v252
	ds_read_b128 v[28:31], v253
	s_and_b64 s[28:29], s[34:35], exec
	ds_read_b128 v[16:19], v252 offset:2048
	ds_read_b128 v[20:23], v253 offset:2048
	s_cselect_b32 s29, s7, s31
	s_cselect_b32 s28, s6, s30
	s_add_u32 s61, s56, s26
	ds_read_b128 v[8:11], v252 offset:16384
	ds_read_b128 v[12:15], v253 offset:16384
	s_addc_u32 s62, s57, s27
	ds_read_b128 v[0:3], v252 offset:18432
	ds_read_b128 v[4:7], v253 offset:18432
	s_and_b64 s[30:31], s[34:35], exec
	s_cselect_b32 s31, s23, s62
	s_cselect_b32 s30, s22, s61
	s_add_u32 s61, s58, s26
	s_addc_u32 s62, s59, s27
	s_and_b64 s[34:35], s[34:35], exec
	s_cselect_b32 s35, s25, s62
	s_cselect_b32 s34, s24, s61
	s_add_u32 s100, s16, s26
	s_addc_u32 s101, s17, s27
	s_add_i32 m0, s37, 0xc000
	ds_read_b128 v[186:189], v206
	ds_read_b128 v[214:217], v206 offset:2048
	ds_read_b128 v[190:193], v207
	ds_read_b128 v[218:221], v207 offset:2048
	ds_read_b128 v[222:225], v206 offset:4096
	ds_read_b128 v[230:233], v206 offset:6144
	ds_read_b128 v[226:229], v207 offset:4096
	ds_read_b128 v[234:237], v207 offset:6144
	global_load_lds_dwordx4 v166, s[100:101]
	s_add_i32 m0, s37, 0xe000
	s_nop 0
	global_load_lds_dwordx4 v168, s[100:101]
	s_waitcnt vmcnt(8)
	s_waitcnt lgkmcnt(0)
	s_barrier
	s_waitcnt lgkmcnt(0)
	v_mfma_f32_16x16x128_f8f6f4 v[156:159], v[24:31], v[186:193], v[156:159]
	v_mfma_f32_16x16x128_f8f6f4 v[152:155], v[16:23], v[186:193], v[152:155]
	v_mfma_f32_16x16x128_f8f6f4 v[136:139], v[16:23], v[214:221], v[136:139]
	v_mfma_f32_16x16x128_f8f6f4 v[144:147], v[24:31], v[214:221], v[144:147]
	v_mfma_f32_16x16x128_f8f6f4 v[128:131], v[24:31], v[222:229], v[128:131]
	v_mfma_f32_16x16x128_f8f6f4 v[120:123], v[16:23], v[222:229], v[120:123]
	v_mfma_f32_16x16x128_f8f6f4 v[104:107], v[16:23], v[230:237], v[104:107]
	v_mfma_f32_16x16x128_f8f6f4 v[112:115], v[24:31], v[230:237], v[112:115]
	v_mfma_f32_16x16x128_f8f6f4 v[148:151], v[8:15], v[186:193], v[148:151]
	v_mfma_f32_16x16x128_f8f6f4 v[140:143], v[0:7], v[186:193], v[140:143]
	v_mfma_f32_16x16x128_f8f6f4 v[124:127], v[0:7], v[214:221], v[124:127]
	v_mfma_f32_16x16x128_f8f6f4 v[132:135], v[8:15], v[214:221], v[132:135]
	v_mfma_f32_16x16x128_f8f6f4 v[116:119], v[8:15], v[222:229], v[116:119]
	v_mfma_f32_16x16x128_f8f6f4 v[108:111], v[0:7], v[222:229], v[108:111]
	v_mfma_f32_16x16x128_f8f6f4 v[96:99], v[0:7], v[230:237], v[96:99]
	v_mfma_f32_16x16x128_f8f6f4 v[100:103], v[8:15], v[230:237], v[100:103]
	s_barrier
	s_add_i32 s61, s44, s36
	s_mov_b32 m0, s61
	ds_read_b128 v[214:217], v206 offset:16384
	ds_read_b128 v[222:225], v206 offset:18432
	ds_read_b128 v[218:221], v207 offset:16384
	ds_read_b128 v[226:229], v207 offset:18432
	ds_read_b128 v[230:233], v206 offset:20480
	ds_read_b128 v[238:241], v206 offset:22528
	ds_read_b128 v[234:237], v207 offset:20480
	ds_read_b128 v[242:245], v207 offset:22528
	global_load_lds_dwordx4 v160, s[30:31]
	s_add_i32 m0, s61, 0x2000
	s_add_i32 s98, s46, s36
	global_load_lds_dwordx4 v162, s[30:31]
	s_mov_b32 m0, s98
	s_nop 0
	global_load_lds_dwordx4 v160, s[34:35]
	s_add_i32 m0, s98, 0x2000
	v_mov_b32_e32 v173, v165
	global_load_lds_dwordx4 v162, s[34:35]
	s_waitcnt vmcnt(6)
	s_waitcnt lgkmcnt(0)
	s_barrier
	s_waitcnt lgkmcnt(0)
	v_mfma_f32_16x16x128_f8f6f4 v[92:95], v[24:31], v[214:221], v[92:95]
	v_mfma_f32_16x16x128_f8f6f4 v[88:91], v[16:23], v[214:221], v[88:91]
	v_mfma_f32_16x16x128_f8f6f4 v[72:75], v[16:23], v[222:229], v[72:75]
	v_mfma_f32_16x16x128_f8f6f4 v[80:83], v[24:31], v[222:229], v[80:83]
	s_mov_b32 m0, s37
	v_mfma_f32_16x16x128_f8f6f4 v[64:67], v[24:31], v[230:237], v[64:67]
	global_load_lds_dwordx4 v164, s[28:29]
	v_mfma_f32_16x16x128_f8f6f4 v[56:59], v[16:23], v[230:237], v[56:59]
	v_mfma_f32_16x16x128_f8f6f4 v[40:43], v[16:23], v[238:245], v[40:43]
	v_mfma_f32_16x16x128_f8f6f4 v[48:51], v[24:31], v[238:245], v[48:51]
	v_mfma_f32_16x16x128_f8f6f4 v[84:87], v[8:15], v[214:221], v[84:87]
	s_mov_b32 m0, s38
	v_mfma_f32_16x16x128_f8f6f4 v[76:79], v[0:7], v[214:221], v[76:79]
	global_load_lds_dwordx4 v172, s[28:29]
	v_mfma_f32_16x16x128_f8f6f4 v[60:63], v[0:7], v[222:229], v[60:63]
	v_mfma_f32_16x16x128_f8f6f4 v[68:71], v[8:15], v[222:229], v[68:71]
	v_mfma_f32_16x16x128_f8f6f4 v[52:55], v[8:15], v[230:237], v[52:55]
	v_mfma_f32_16x16x128_f8f6f4 v[44:47], v[0:7], v[230:237], v[44:47]
	v_mfma_f32_16x16x128_f8f6f4 v[32:35], v[0:7], v[238:245], v[32:35]
	v_mfma_f32_16x16x128_f8f6f4 v[36:39], v[8:15], v[238:245], v[36:39]
	s_barrier
	ds_read_b128 v[0:3], v252 offset:32768
	ds_read_b128 v[4:7], v253 offset:32768
	ds_read_b128 v[8:11], v252 offset:34816
	ds_read_b128 v[12:15], v253 offset:34816
	ds_read_b128 v[16:19], v252 offset:49152
	ds_read_b128 v[20:23], v253 offset:49152
	ds_read_b128 v[24:27], v252 offset:51200
	ds_read_b128 v[28:31], v253 offset:51200
	s_mov_b32 m0, s39
	ds_read_b128 v[214:217], v206 offset:32768
	ds_read_b128 v[222:225], v206 offset:34816
	ds_read_b128 v[218:221], v207 offset:32768
	ds_read_b128 v[226:229], v207 offset:34816
	ds_read_b128 v[230:233], v206 offset:36864
	ds_read_b128 v[238:241], v206 offset:38912
	ds_read_b128 v[234:237], v207 offset:36864
	ds_read_b128 v[242:245], v207 offset:38912
	global_load_lds_dwordx4 v184, s[28:29]
	s_mov_b32 m0, s40
	s_nop 0
	global_load_lds_dwordx4 v182, s[28:29]
	s_waitcnt vmcnt(8)
	s_waitcnt lgkmcnt(0)
	s_barrier
	s_waitcnt lgkmcnt(0)
	v_mfma_f32_16x16x128_f8f6f4 v[156:159], v[0:7], v[214:221], v[156:159]
	v_mfma_f32_16x16x128_f8f6f4 v[152:155], v[8:15], v[214:221], v[152:155]
	v_mfma_f32_16x16x128_f8f6f4 v[136:139], v[8:15], v[222:229], v[136:139]
	v_mfma_f32_16x16x128_f8f6f4 v[144:147], v[0:7], v[222:229], v[144:147]
	v_mfma_f32_16x16x128_f8f6f4 v[128:131], v[0:7], v[230:237], v[128:131]
	v_mfma_f32_16x16x128_f8f6f4 v[120:123], v[8:15], v[230:237], v[120:123]
	v_mfma_f32_16x16x128_f8f6f4 v[104:107], v[8:15], v[238:245], v[104:107]
	v_mfma_f32_16x16x128_f8f6f4 v[112:115], v[0:7], v[238:245], v[112:115]
	v_mfma_f32_16x16x128_f8f6f4 v[148:151], v[16:23], v[214:221], v[148:151]
	v_mfma_f32_16x16x128_f8f6f4 v[140:143], v[24:31], v[214:221], v[140:143]
	v_mfma_f32_16x16x128_f8f6f4 v[124:127], v[24:31], v[222:229], v[124:127]
	v_mfma_f32_16x16x128_f8f6f4 v[132:135], v[16:23], v[222:229], v[132:135]
	v_mfma_f32_16x16x128_f8f6f4 v[116:119], v[16:23], v[230:237], v[116:119]
	v_mfma_f32_16x16x128_f8f6f4 v[108:111], v[24:31], v[230:237], v[108:111]
	v_mfma_f32_16x16x128_f8f6f4 v[96:99], v[24:31], v[238:245], v[96:99]
	v_mfma_f32_16x16x128_f8f6f4 v[100:103], v[16:23], v[238:245], v[100:103]
	s_barrier
	s_add_i32 s99, s36, 0x17f80
	s_mov_b32 m0, s99
	ds_read_b128 v[214:217], v206 offset:49152
	ds_read_b128 v[222:225], v206 offset:51200
	ds_read_b128 v[218:221], v207 offset:49152
	ds_read_b128 v[226:229], v207 offset:51200
	ds_read_b128 v[230:233], v206 offset:53248
	ds_read_b128 v[238:241], v206 offset:55296
	ds_read_b128 v[234:237], v207 offset:53248
	ds_read_b128 v[242:245], v207 offset:55296
	global_load_lds_dwordx4 v160, s[30:31] offset:128
	s_add_i32 m0, s99, 0x2000
	s_add_i32 s99, s36, 0x1bf80
	global_load_lds_dwordx4 v162, s[30:31] offset:128
	s_mov_b32 m0, s99
	s_nop 0
	global_load_lds_dwordx4 v160, s[34:35] offset:128
	s_add_i32 m0, s99, 0x2000
	s_nop 0
	global_load_lds_dwordx4 v162, s[34:35] offset:128
	s_waitcnt vmcnt(6)
	s_waitcnt lgkmcnt(0)
	s_barrier
	s_waitcnt lgkmcnt(0)
	v_mfma_f32_16x16x128_f8f6f4 v[92:95], v[0:7], v[214:221], v[92:95]
	v_mfma_f32_16x16x128_f8f6f4 v[88:91], v[8:15], v[214:221], v[88:91]
	v_mfma_f32_16x16x128_f8f6f4 v[72:75], v[8:15], v[222:229], v[72:75]
	v_mfma_f32_16x16x128_f8f6f4 v[80:83], v[0:7], v[222:229], v[80:83]
	s_add_i32 m0, s41, 0xffffff80
	v_mfma_f32_16x16x128_f8f6f4 v[64:67], v[0:7], v[230:237], v[64:67]
	global_load_lds_dwordx4 v164, s[28:29] offset:128
	v_mfma_f32_16x16x128_f8f6f4 v[56:59], v[8:15], v[230:237], v[56:59]
	v_mfma_f32_16x16x128_f8f6f4 v[40:43], v[8:15], v[238:245], v[40:43]
	v_mfma_f32_16x16x128_f8f6f4 v[48:51], v[0:7], v[238:245], v[48:51]
	v_mfma_f32_16x16x128_f8f6f4 v[84:87], v[16:23], v[214:221], v[84:87]
	s_add_i32 m0, s42, 0xffffff80
	v_mfma_f32_16x16x128_f8f6f4 v[76:79], v[24:31], v[214:221], v[76:79]
	global_load_lds_dwordx4 v172, s[28:29] offset:128
	v_mfma_f32_16x16x128_f8f6f4 v[60:63], v[24:31], v[222:229], v[60:63]
	v_mfma_f32_16x16x128_f8f6f4 v[68:71], v[16:23], v[222:229], v[68:71]
	v_mfma_f32_16x16x128_f8f6f4 v[52:55], v[16:23], v[230:237], v[52:55]
	v_mfma_f32_16x16x128_f8f6f4 v[44:47], v[24:31], v[230:237], v[44:47]
	v_mfma_f32_16x16x128_f8f6f4 v[32:35], v[24:31], v[238:245], v[32:35]
	v_mfma_f32_16x16x128_f8f6f4 v[36:39], v[16:23], v[238:245], v[36:39]
	s_barrier
	s_add_i32 s60, s60, 2
	s_add_u32 s26, s26, 0x100
	s_addc_u32 s27, s27, 0
	s_cmp_gt_u32 s60, 5
	s_cbranch_scc1 .LBB0_180

.LBB0_430:
	s_add_u32 s26, s4, s24
	s_addc_u32 s27, s5, s25
	s_add_u32 s30, s26, 0x21c00100
	s_addc_u32 s31, s27, 0
	ds_read_b128 v[172:175], v252
	ds_read_b128 v[176:179], v253
	s_and_b64 s[26:27], s[28:29], exec
	ds_read_b128 v[180:183], v252 offset:2048
	ds_read_b128 v[184:187], v253 offset:2048
	s_cselect_b32 s27, s7, s31
	s_cselect_b32 s26, s6, s30
	s_add_u32 s65, s60, s24
	ds_read_b128 v[188:191], v252 offset:16384
	ds_read_b128 v[192:195], v253 offset:16384
	s_addc_u32 s66, s61, s25
	ds_read_b128 v[196:199], v252 offset:18432
	ds_read_b128 v[200:203], v253 offset:18432
	s_and_b64 s[30:31], s[28:29], exec
	s_cselect_b32 s31, s21, s66
	s_cselect_b32 s30, s20, s65
	s_add_u32 s65, s62, s24
	s_addc_u32 s66, s63, s25
	s_and_b64 s[28:29], s[28:29], exec
	s_cselect_b32 s29, s23, s66
	s_cselect_b32 s28, s22, s65
	v_lshl_add_u64 v[236:237], v[156:157], 0, s[24:25]
	s_add_i32 m0, s37, 0xc000
	ds_read_b128 v[204:207], v169
	ds_read_b128 v[208:211], v169 offset:1024
	ds_read_b128 v[212:215], v169 offset:2048
	ds_read_b128 v[216:219], v169 offset:3072
	ds_read_b128 v[220:223], v169 offset:4096
	ds_read_b128 v[224:227], v169 offset:5120
	ds_read_b128 v[228:231], v169 offset:6144
	ds_read_b128 v[232:235], v169 offset:7168
	global_load_lds_dwordx4 v[236:237], off
	v_lshl_add_u64 v[236:237], v[154:155], 0, s[24:25]
	s_add_i32 m0, s37, 0xe000
	s_nop 0
	global_load_lds_dwordx4 v[236:237], off
	s_waitcnt vmcnt(8)
	s_waitcnt lgkmcnt(0)
	s_barrier
	s_waitcnt lgkmcnt(0)
	v_mfma_f32_16x16x32_bf16 v[140:143], v[172:175], v[204:207], v[140:143]
	v_mfma_f32_16x16x32_bf16 v[136:139], v[180:183], v[204:207], v[136:139]
	v_mfma_f32_16x16x32_bf16 v[124:127], v[172:175], v[212:215], v[124:127]
	v_mfma_f32_16x16x32_bf16 v[120:123], v[180:183], v[212:215], v[120:123]
	v_mfma_f32_16x16x32_bf16 v[92:95], v[172:175], v[220:223], v[92:95]
	v_mfma_f32_16x16x32_bf16 v[88:91], v[180:183], v[220:223], v[88:91]
	v_mfma_f32_16x16x32_bf16 v[76:79], v[172:175], v[228:231], v[76:79]
	v_mfma_f32_16x16x32_bf16 v[72:75], v[180:183], v[228:231], v[72:75]
	v_mfma_f32_16x16x32_bf16 v[140:143], v[176:179], v[208:211], v[140:143]
	v_mfma_f32_16x16x32_bf16 v[136:139], v[184:187], v[208:211], v[136:139]
	v_mfma_f32_16x16x32_bf16 v[124:127], v[176:179], v[216:219], v[124:127]
	v_mfma_f32_16x16x32_bf16 v[120:123], v[184:187], v[216:219], v[120:123]
	v_mfma_f32_16x16x32_bf16 v[92:95], v[176:179], v[224:227], v[92:95]
	v_mfma_f32_16x16x32_bf16 v[88:91], v[184:187], v[224:227], v[88:91]
	v_mfma_f32_16x16x32_bf16 v[76:79], v[176:179], v[232:235], v[76:79]
	v_mfma_f32_16x16x32_bf16 v[72:75], v[184:187], v[232:235], v[72:75]
	v_mfma_f32_16x16x32_bf16 v[132:135], v[188:191], v[204:207], v[132:135]
	v_mfma_f32_16x16x32_bf16 v[128:131], v[196:199], v[204:207], v[128:131]
	v_mfma_f32_16x16x32_bf16 v[108:111], v[188:191], v[212:215], v[108:111]
	v_mfma_f32_16x16x32_bf16 v[96:99], v[196:199], v[212:215], v[96:99]
	v_mfma_f32_16x16x32_bf16 v[84:87], v[188:191], v[220:223], v[84:87]
	v_mfma_f32_16x16x32_bf16 v[80:83], v[196:199], v[220:223], v[80:83]
	v_mfma_f32_16x16x32_bf16 v[68:71], v[188:191], v[228:231], v[68:71]
	v_mfma_f32_16x16x32_bf16 v[64:67], v[196:199], v[228:231], v[64:67]
	v_mfma_f32_16x16x32_bf16 v[132:135], v[192:195], v[208:211], v[132:135]
	v_mfma_f32_16x16x32_bf16 v[128:131], v[200:203], v[208:211], v[128:131]
	v_mfma_f32_16x16x32_bf16 v[108:111], v[192:195], v[216:219], v[108:111]
	v_mfma_f32_16x16x32_bf16 v[96:99], v[200:203], v[216:219], v[96:99]
	v_mfma_f32_16x16x32_bf16 v[84:87], v[192:195], v[224:227], v[84:87]
	v_mfma_f32_16x16x32_bf16 v[80:83], v[200:203], v[224:227], v[80:83]
	v_mfma_f32_16x16x32_bf16 v[68:71], v[192:195], v[232:235], v[68:71]
	v_mfma_f32_16x16x32_bf16 v[64:67], v[200:203], v[232:235], v[64:67]
	s_barrier
	s_add_i32 s65, s48, s35
	v_lshl_add_u64 v[236:237], s[30:31], 0, v[146:147]
	s_mov_b32 m0, s65
	ds_read_b128 v[204:207], v169 offset:16384
	ds_read_b128 v[208:211], v169 offset:17408
	ds_read_b128 v[212:215], v169 offset:18432
	ds_read_b128 v[216:219], v169 offset:19456
	ds_read_b128 v[220:223], v169 offset:20480
	ds_read_b128 v[224:227], v169 offset:21504
	ds_read_b128 v[228:231], v169 offset:22528
	ds_read_b128 v[232:235], v169 offset:23552
	global_load_lds_dwordx4 v[236:237], off
	v_lshl_add_u64 v[238:239], s[30:31], 0, v[148:149]
	s_add_i32 m0, s65, 0x2000
	s_add_i32 s30, s50, s35
	global_load_lds_dwordx4 v[238:239], off
	v_lshl_add_u64 v[240:241], s[28:29], 0, v[146:147]
	s_mov_b32 m0, s30
	v_lshl_add_u64 v[242:243], s[28:29], 0, v[148:149]
	global_load_lds_dwordx4 v[240:241], off
	s_add_i32 m0, s30, 0x2000
	v_mov_b32_e32 v153, v151
	global_load_lds_dwordx4 v[242:243], off
	s_mov_b32 m0, s37
	v_lshl_add_u64 v[244:245], s[26:27], 0, v[150:151]
	global_load_lds_dwordx4 v150, s[26:27]
	s_mov_b32 m0, s38
	v_lshl_add_u64 v[246:247], s[26:27], 0, v[152:153]
	global_load_lds_dwordx4 v152, s[26:27]
	s_waitcnt vmcnt(8)
	s_waitcnt lgkmcnt(0)
	s_barrier
	s_waitcnt lgkmcnt(0)
	v_mfma_f32_16x16x32_bf16 v[60:63], v[172:175], v[204:207], v[60:63]
	v_mfma_f32_16x16x32_bf16 v[56:59], v[180:183], v[204:207], v[56:59]
	v_mfma_f32_16x16x32_bf16 v[44:47], v[172:175], v[212:215], v[44:47]
	v_mfma_f32_16x16x32_bf16 v[40:43], v[180:183], v[212:215], v[40:43]
	v_mfma_f32_16x16x32_bf16 v[28:31], v[172:175], v[220:223], v[28:31]
	v_mfma_f32_16x16x32_bf16 v[24:27], v[180:183], v[220:223], v[24:27]
	v_mfma_f32_16x16x32_bf16 v[12:15], v[172:175], v[228:231], v[12:15]
	v_mfma_f32_16x16x32_bf16 v[8:11], v[180:183], v[228:231], v[8:11]
	v_mfma_f32_16x16x32_bf16 v[60:63], v[176:179], v[208:211], v[60:63]
	v_mfma_f32_16x16x32_bf16 v[56:59], v[184:187], v[208:211], v[56:59]
	v_mfma_f32_16x16x32_bf16 v[44:47], v[176:179], v[216:219], v[44:47]
	v_mfma_f32_16x16x32_bf16 v[40:43], v[184:187], v[216:219], v[40:43]
	v_mfma_f32_16x16x32_bf16 v[28:31], v[176:179], v[224:227], v[28:31]
	v_mfma_f32_16x16x32_bf16 v[24:27], v[184:187], v[224:227], v[24:27]
	v_mfma_f32_16x16x32_bf16 v[12:15], v[176:179], v[232:235], v[12:15]
	v_mfma_f32_16x16x32_bf16 v[8:11], v[184:187], v[232:235], v[8:11]
	v_mfma_f32_16x16x32_bf16 v[52:55], v[188:191], v[204:207], v[52:55]
	v_mfma_f32_16x16x32_bf16 v[48:51], v[196:199], v[204:207], v[48:51]
	v_mfma_f32_16x16x32_bf16 v[36:39], v[188:191], v[212:215], v[36:39]
	v_mfma_f32_16x16x32_bf16 v[32:35], v[196:199], v[212:215], v[32:35]
	v_mfma_f32_16x16x32_bf16 v[20:23], v[188:191], v[220:223], v[20:23]
	v_mfma_f32_16x16x32_bf16 v[16:19], v[196:199], v[220:223], v[16:19]
	v_mfma_f32_16x16x32_bf16 v[4:7], v[188:191], v[228:231], v[4:7]
	v_mfma_f32_16x16x32_bf16 v[0:3], v[196:199], v[228:231], v[0:3]
	v_mfma_f32_16x16x32_bf16 v[52:55], v[192:195], v[208:211], v[52:55]
	v_mfma_f32_16x16x32_bf16 v[48:51], v[200:203], v[208:211], v[48:51]
	v_mfma_f32_16x16x32_bf16 v[36:39], v[192:195], v[216:219], v[36:39]
	v_mfma_f32_16x16x32_bf16 v[32:35], v[200:203], v[216:219], v[32:35]
	v_mfma_f32_16x16x32_bf16 v[20:23], v[192:195], v[224:227], v[20:23]
	v_mfma_f32_16x16x32_bf16 v[16:19], v[200:203], v[224:227], v[16:19]
	v_mfma_f32_16x16x32_bf16 v[4:7], v[192:195], v[232:235], v[4:7]
	v_mfma_f32_16x16x32_bf16 v[0:3], v[200:203], v[232:235], v[0:3]
	s_barrier
	s_add_i32 s28, 0, 0x18000
	ds_read_b128 v[172:175], v252 offset:32768
	ds_read_b128 v[176:179], v253 offset:32768
	s_add_i32 s29, 0, 0x1c000
	ds_read_b128 v[180:183], v252 offset:34816
	ds_read_b128 v[184:187], v253 offset:34816
	ds_read_b128 v[188:191], v252 offset:49152
	ds_read_b128 v[192:195], v253 offset:49152
	ds_read_b128 v[196:199], v252 offset:51200
	ds_read_b128 v[200:203], v253 offset:51200
	s_mov_b32 m0, s39
	v_lshl_add_u64 v[160:161], s[26:27], 0, v[160:161]
	ds_read_b128 v[204:207], v169 offset:32768
	ds_read_b128 v[208:211], v169 offset:33792
	ds_read_b128 v[212:215], v169 offset:34816
	ds_read_b128 v[216:219], v169 offset:35840
	ds_read_b128 v[220:223], v169 offset:36864
	ds_read_b128 v[224:227], v169 offset:37888
	ds_read_b128 v[228:231], v169 offset:38912
	ds_read_b128 v[232:235], v169 offset:39936
	global_load_lds_dwordx4 v[160:161], off
	v_lshl_add_u64 v[158:159], s[26:27], 0, v[158:159]
	s_mov_b32 m0, s40
	s_nop 0
	global_load_lds_dwordx4 v[158:159], off
	s_waitcnt vmcnt(8)
	s_waitcnt lgkmcnt(0)
	s_barrier
	s_waitcnt lgkmcnt(0)
	v_mfma_f32_16x16x32_bf16 v[140:143], v[172:175], v[204:207], v[140:143]
	v_mfma_f32_16x16x32_bf16 v[136:139], v[180:183], v[204:207], v[136:139]
	v_mfma_f32_16x16x32_bf16 v[124:127], v[172:175], v[212:215], v[124:127]
	v_mfma_f32_16x16x32_bf16 v[120:123], v[180:183], v[212:215], v[120:123]
	v_mfma_f32_16x16x32_bf16 v[92:95], v[172:175], v[220:223], v[92:95]
	v_mfma_f32_16x16x32_bf16 v[88:91], v[180:183], v[220:223], v[88:91]
	v_mfma_f32_16x16x32_bf16 v[76:79], v[172:175], v[228:231], v[76:79]
	v_mfma_f32_16x16x32_bf16 v[72:75], v[180:183], v[228:231], v[72:75]
	v_mfma_f32_16x16x32_bf16 v[140:143], v[176:179], v[208:211], v[140:143]
	v_mfma_f32_16x16x32_bf16 v[136:139], v[184:187], v[208:211], v[136:139]
	v_mfma_f32_16x16x32_bf16 v[124:127], v[176:179], v[216:219], v[124:127]
	v_mfma_f32_16x16x32_bf16 v[120:123], v[184:187], v[216:219], v[120:123]
	v_mfma_f32_16x16x32_bf16 v[92:95], v[176:179], v[224:227], v[92:95]
	v_mfma_f32_16x16x32_bf16 v[88:91], v[184:187], v[224:227], v[88:91]
	v_mfma_f32_16x16x32_bf16 v[76:79], v[176:179], v[232:235], v[76:79]
	v_mfma_f32_16x16x32_bf16 v[72:75], v[184:187], v[232:235], v[72:75]
	v_mfma_f32_16x16x32_bf16 v[132:135], v[188:191], v[204:207], v[132:135]
	v_mfma_f32_16x16x32_bf16 v[128:131], v[196:199], v[204:207], v[128:131]
	v_mfma_f32_16x16x32_bf16 v[108:111], v[188:191], v[212:215], v[108:111]
	v_mfma_f32_16x16x32_bf16 v[96:99], v[196:199], v[212:215], v[96:99]
	v_mfma_f32_16x16x32_bf16 v[84:87], v[188:191], v[220:223], v[84:87]
	v_mfma_f32_16x16x32_bf16 v[80:83], v[196:199], v[220:223], v[80:83]
	v_mfma_f32_16x16x32_bf16 v[68:71], v[188:191], v[228:231], v[68:71]
	v_mfma_f32_16x16x32_bf16 v[64:67], v[196:199], v[228:231], v[64:67]
	v_mfma_f32_16x16x32_bf16 v[132:135], v[192:195], v[208:211], v[132:135]
	v_mfma_f32_16x16x32_bf16 v[128:131], v[200:203], v[208:211], v[128:131]
	v_mfma_f32_16x16x32_bf16 v[108:111], v[192:195], v[216:219], v[108:111]
	v_mfma_f32_16x16x32_bf16 v[96:99], v[200:203], v[216:219], v[96:99]
	v_mfma_f32_16x16x32_bf16 v[84:87], v[192:195], v[224:227], v[84:87]
	v_mfma_f32_16x16x32_bf16 v[80:83], v[200:203], v[224:227], v[80:83]
	v_mfma_f32_16x16x32_bf16 v[68:71], v[192:195], v[232:235], v[68:71]
	v_mfma_f32_16x16x32_bf16 v[64:67], v[200:203], v[232:235], v[64:67]
	s_barrier
	s_add_i32 s26, s28, s35
	v_lshl_add_u64 v[232:233], v[236:237], 0, s[14:15]
	s_mov_b32 m0, s26
	ds_read_b128 v[158:161], v169 offset:49152
	ds_read_b128 v[204:207], v169 offset:50176
	ds_read_b128 v[208:211], v169 offset:51200
	ds_read_b128 v[212:215], v169 offset:52224
	ds_read_b128 v[216:219], v169 offset:53248
	ds_read_b128 v[220:223], v169 offset:54272
	ds_read_b128 v[224:227], v169 offset:55296
	ds_read_b128 v[228:231], v169 offset:56320
	global_load_lds_dwordx4 v[232:233], off
	v_lshl_add_u64 v[232:233], v[238:239], 0, s[14:15]
	s_add_i32 m0, s26, 0x2000
	s_add_i32 s26, s29, s35
	global_load_lds_dwordx4 v[232:233], off
	v_lshl_add_u64 v[232:233], v[240:241], 0, s[14:15]
	s_mov_b32 m0, s26
	s_nop 0
	global_load_lds_dwordx4 v[232:233], off
	v_lshl_add_u64 v[232:233], v[242:243], 0, s[14:15]
	s_add_i32 m0, s26, 0x2000
	s_nop 0
	global_load_lds_dwordx4 v[232:233], off
	v_lshl_add_u64 v[232:233], v[244:245], 0, s[14:15]
	s_mov_b32 m0, s45
	s_nop 0
	global_load_lds_dwordx4 v[232:233], off
	v_lshl_add_u64 v[232:233], v[246:247], 0, s[14:15]
	s_mov_b32 m0, s46
	s_nop 0
	global_load_lds_dwordx4 v[232:233], off
	s_waitcnt vmcnt(8)
	s_waitcnt lgkmcnt(0)
	s_barrier
	s_waitcnt lgkmcnt(0)
	v_mfma_f32_16x16x32_bf16 v[60:63], v[172:175], v[158:161], v[60:63]
	v_mfma_f32_16x16x32_bf16 v[56:59], v[180:183], v[158:161], v[56:59]
	v_mfma_f32_16x16x32_bf16 v[44:47], v[172:175], v[208:211], v[44:47]
	v_mfma_f32_16x16x32_bf16 v[40:43], v[180:183], v[208:211], v[40:43]
	v_mfma_f32_16x16x32_bf16 v[28:31], v[172:175], v[216:219], v[28:31]
	v_mfma_f32_16x16x32_bf16 v[24:27], v[180:183], v[216:219], v[24:27]
	v_mfma_f32_16x16x32_bf16 v[12:15], v[172:175], v[224:227], v[12:15]
	v_mfma_f32_16x16x32_bf16 v[8:11], v[180:183], v[224:227], v[8:11]
	v_mfma_f32_16x16x32_bf16 v[60:63], v[176:179], v[204:207], v[60:63]
	v_mfma_f32_16x16x32_bf16 v[56:59], v[184:187], v[204:207], v[56:59]
	v_mfma_f32_16x16x32_bf16 v[44:47], v[176:179], v[212:215], v[44:47]
	v_mfma_f32_16x16x32_bf16 v[40:43], v[184:187], v[212:215], v[40:43]
	v_mfma_f32_16x16x32_bf16 v[28:31], v[176:179], v[220:223], v[28:31]
	v_mfma_f32_16x16x32_bf16 v[24:27], v[184:187], v[220:223], v[24:27]
	v_mfma_f32_16x16x32_bf16 v[12:15], v[176:179], v[228:231], v[12:15]
	v_mfma_f32_16x16x32_bf16 v[8:11], v[184:187], v[228:231], v[8:11]
	v_mfma_f32_16x16x32_bf16 v[52:55], v[188:191], v[158:161], v[52:55]
	v_mfma_f32_16x16x32_bf16 v[48:51], v[196:199], v[158:161], v[48:51]
	v_mfma_f32_16x16x32_bf16 v[36:39], v[188:191], v[208:211], v[36:39]
	v_mfma_f32_16x16x32_bf16 v[32:35], v[196:199], v[208:211], v[32:35]
	v_mfma_f32_16x16x32_bf16 v[20:23], v[188:191], v[216:219], v[20:23]
	v_mfma_f32_16x16x32_bf16 v[16:19], v[196:199], v[216:219], v[16:19]
	v_mfma_f32_16x16x32_bf16 v[4:7], v[188:191], v[224:227], v[4:7]
	v_mfma_f32_16x16x32_bf16 v[0:3], v[196:199], v[224:227], v[0:3]
	v_mfma_f32_16x16x32_bf16 v[52:55], v[192:195], v[204:207], v[52:55]
	v_mfma_f32_16x16x32_bf16 v[48:51], v[200:203], v[204:207], v[48:51]
	v_mfma_f32_16x16x32_bf16 v[36:39], v[192:195], v[212:215], v[36:39]
	v_mfma_f32_16x16x32_bf16 v[32:35], v[200:203], v[212:215], v[32:35]
	v_mfma_f32_16x16x32_bf16 v[20:23], v[192:195], v[220:223], v[20:23]
	v_mfma_f32_16x16x32_bf16 v[16:19], v[200:203], v[220:223], v[16:19]
	v_mfma_f32_16x16x32_bf16 v[4:7], v[192:195], v[228:231], v[4:7]
	v_mfma_f32_16x16x32_bf16 v[0:3], v[200:203], v[228:231], v[0:3]
	s_barrier
	s_add_i32 s64, s64, 2
	s_add_u32 s24, s24, 0x100
	s_addc_u32 s25, s25, 0
	s_cmp_gt_u32 s64, 9
	s_cbranch_scc1 .LBB0_433

.LBB0_590:
	s_add_u32 s36, s8, s4
	s_addc_u32 s37, s9, s5
	s_add_u32 s38, s36, 0xe000100
	s_addc_u32 s39, s37, 0
	ds_read_b128 v[24:27], v252
	ds_read_b128 v[28:31], v253
	s_and_b64 s[36:37], s[40:41], exec
	ds_read_b128 v[16:19], v252 offset:2048
	ds_read_b128 v[20:23], v253 offset:2048
	s_cselect_b32 s37, s11, s39
	s_cselect_b32 s36, s10, s38
	s_add_u32 s90, s27, s4
	ds_read_b128 v[8:11], v252 offset:16384
	ds_read_b128 v[12:15], v253 offset:16384
	s_addc_u32 s91, s86, s5
	ds_read_b128 v[0:3], v252 offset:18432
	ds_read_b128 v[4:7], v253 offset:18432
	s_and_b64 s[38:39], s[40:41], exec
	s_cselect_b32 s39, s29, s91
	s_cselect_b32 s38, s28, s90
	s_add_u32 s90, s87, s4
	s_addc_u32 s91, s88, s5
	s_and_b64 s[40:41], s[40:41], exec
	s_cselect_b32 s41, s31, s91
	s_cselect_b32 s40, s30, s90
	s_add_u32 s100, s18, s4
	s_addc_u32 s101, s19, s5
	s_add_i32 m0, s61, 0xc000
	ds_read_b128 v[182:185], v201
	ds_read_b128 v[210:213], v201 offset:2048
	ds_read_b128 v[186:189], v202
	ds_read_b128 v[214:217], v202 offset:2048
	ds_read_b128 v[218:221], v201 offset:4096
	ds_read_b128 v[226:229], v201 offset:6144
	ds_read_b128 v[222:225], v202 offset:4096
	ds_read_b128 v[230:233], v202 offset:6144
	global_load_lds_dwordx4 v170, s[100:101]
	s_add_i32 m0, s61, 0xe000
	s_nop 0
	global_load_lds_dwordx4 v168, s[100:101]
	s_waitcnt vmcnt(8)
	s_waitcnt lgkmcnt(0)
	s_barrier
	s_waitcnt lgkmcnt(0)
	v_mfma_f32_16x16x128_f8f6f4 v[156:159], v[24:31], v[182:189], v[156:159]
	v_mfma_f32_16x16x128_f8f6f4 v[148:151], v[16:23], v[182:189], v[148:151]
	v_mfma_f32_16x16x128_f8f6f4 v[132:135], v[16:23], v[210:217], v[132:135]
	v_mfma_f32_16x16x128_f8f6f4 v[140:143], v[24:31], v[210:217], v[140:143]
	v_mfma_f32_16x16x128_f8f6f4 v[124:127], v[24:31], v[218:225], v[124:127]
	v_mfma_f32_16x16x128_f8f6f4 v[116:119], v[16:23], v[218:225], v[116:119]
	v_mfma_f32_16x16x128_f8f6f4 v[100:103], v[16:23], v[226:233], v[100:103]
	v_mfma_f32_16x16x128_f8f6f4 v[108:111], v[24:31], v[226:233], v[108:111]
	v_mfma_f32_16x16x128_f8f6f4 v[152:155], v[8:15], v[182:189], v[152:155]
	v_mfma_f32_16x16x128_f8f6f4 v[144:147], v[0:7], v[182:189], v[144:147]
	v_mfma_f32_16x16x128_f8f6f4 v[128:131], v[0:7], v[210:217], v[128:131]
	v_mfma_f32_16x16x128_f8f6f4 v[136:139], v[8:15], v[210:217], v[136:139]
	v_mfma_f32_16x16x128_f8f6f4 v[120:123], v[8:15], v[218:225], v[120:123]
	v_mfma_f32_16x16x128_f8f6f4 v[112:115], v[0:7], v[218:225], v[112:115]
	v_mfma_f32_16x16x128_f8f6f4 v[96:99], v[0:7], v[226:233], v[96:99]
	v_mfma_f32_16x16x128_f8f6f4 v[104:107], v[8:15], v[226:233], v[104:107]
	s_barrier
	s_add_i32 s90, s72, s44
	s_mov_b32 m0, s90
	ds_read_b128 v[210:213], v201 offset:16384
	ds_read_b128 v[218:221], v201 offset:18432
	ds_read_b128 v[214:217], v202 offset:16384
	ds_read_b128 v[222:225], v202 offset:18432
	ds_read_b128 v[226:229], v201 offset:20480
	ds_read_b128 v[234:237], v201 offset:22528
	ds_read_b128 v[230:233], v202 offset:20480
	ds_read_b128 v[238:241], v202 offset:22528
	global_load_lds_dwordx4 v160, s[38:39]
	s_add_i32 m0, s90, 0x2000
	s_add_i32 s98, s74, s44
	global_load_lds_dwordx4 v162, s[38:39]
	s_mov_b32 m0, s98
	s_nop 0
	global_load_lds_dwordx4 v160, s[40:41]
	s_add_i32 m0, s98, 0x2000
	v_mov_b32_e32 v167, v165
	global_load_lds_dwordx4 v162, s[40:41]
	s_waitcnt vmcnt(6)
	s_waitcnt lgkmcnt(0)
	s_barrier
	s_waitcnt lgkmcnt(0)
	v_mfma_f32_16x16x128_f8f6f4 v[92:95], v[24:31], v[210:217], v[92:95]
	v_mfma_f32_16x16x128_f8f6f4 v[84:87], v[16:23], v[210:217], v[84:87]
	v_mfma_f32_16x16x128_f8f6f4 v[68:71], v[16:23], v[218:225], v[68:71]
	v_mfma_f32_16x16x128_f8f6f4 v[76:79], v[24:31], v[218:225], v[76:79]
	s_mov_b32 m0, s61
	v_mfma_f32_16x16x128_f8f6f4 v[60:63], v[24:31], v[226:233], v[60:63]
	global_load_lds_dwordx4 v164, s[36:37]
	v_mfma_f32_16x16x128_f8f6f4 v[52:55], v[16:23], v[226:233], v[52:55]
	v_mfma_f32_16x16x128_f8f6f4 v[36:39], v[16:23], v[234:241], v[36:39]
	v_mfma_f32_16x16x128_f8f6f4 v[44:47], v[24:31], v[234:241], v[44:47]
	v_mfma_f32_16x16x128_f8f6f4 v[88:91], v[8:15], v[210:217], v[88:91]
	s_mov_b32 m0, s62
	v_mfma_f32_16x16x128_f8f6f4 v[80:83], v[0:7], v[210:217], v[80:83]
	global_load_lds_dwordx4 v166, s[36:37]
	v_mfma_f32_16x16x128_f8f6f4 v[64:67], v[0:7], v[218:225], v[64:67]
	v_mfma_f32_16x16x128_f8f6f4 v[72:75], v[8:15], v[218:225], v[72:75]
	v_mfma_f32_16x16x128_f8f6f4 v[56:59], v[8:15], v[226:233], v[56:59]
	v_mfma_f32_16x16x128_f8f6f4 v[48:51], v[0:7], v[226:233], v[48:51]
	v_mfma_f32_16x16x128_f8f6f4 v[32:35], v[0:7], v[234:241], v[32:35]
	v_mfma_f32_16x16x128_f8f6f4 v[40:43], v[8:15], v[234:241], v[40:43]
	s_barrier
	ds_read_b128 v[0:3], v252 offset:32768
	ds_read_b128 v[4:7], v253 offset:32768
	ds_read_b128 v[8:11], v252 offset:34816
	ds_read_b128 v[12:15], v253 offset:34816
	ds_read_b128 v[16:19], v252 offset:49152
	ds_read_b128 v[20:23], v253 offset:49152
	ds_read_b128 v[24:27], v252 offset:51200
	ds_read_b128 v[28:31], v253 offset:51200
	s_mov_b32 m0, s63
	ds_read_b128 v[210:213], v201 offset:32768
	ds_read_b128 v[218:221], v201 offset:34816
	ds_read_b128 v[214:217], v202 offset:32768
	ds_read_b128 v[222:225], v202 offset:34816
	ds_read_b128 v[226:229], v201 offset:36864
	ds_read_b128 v[234:237], v201 offset:38912
	ds_read_b128 v[230:233], v202 offset:36864
	ds_read_b128 v[238:241], v202 offset:38912
	global_load_lds_dwordx4 v180, s[36:37]
	s_mov_b32 m0, s64
	s_nop 0
	global_load_lds_dwordx4 v178, s[36:37]
	s_waitcnt vmcnt(8)
	s_waitcnt lgkmcnt(0)
	s_barrier
	s_waitcnt lgkmcnt(0)
	v_mfma_f32_16x16x128_f8f6f4 v[156:159], v[0:7], v[210:217], v[156:159]
	v_mfma_f32_16x16x128_f8f6f4 v[148:151], v[8:15], v[210:217], v[148:151]
	v_mfma_f32_16x16x128_f8f6f4 v[132:135], v[8:15], v[218:225], v[132:135]
	v_mfma_f32_16x16x128_f8f6f4 v[140:143], v[0:7], v[218:225], v[140:143]
	v_mfma_f32_16x16x128_f8f6f4 v[124:127], v[0:7], v[226:233], v[124:127]
	v_mfma_f32_16x16x128_f8f6f4 v[116:119], v[8:15], v[226:233], v[116:119]
	v_mfma_f32_16x16x128_f8f6f4 v[100:103], v[8:15], v[234:241], v[100:103]
	v_mfma_f32_16x16x128_f8f6f4 v[108:111], v[0:7], v[234:241], v[108:111]
	v_mfma_f32_16x16x128_f8f6f4 v[152:155], v[16:23], v[210:217], v[152:155]
	v_mfma_f32_16x16x128_f8f6f4 v[144:147], v[24:31], v[210:217], v[144:147]
	v_mfma_f32_16x16x128_f8f6f4 v[128:131], v[24:31], v[218:225], v[128:131]
	v_mfma_f32_16x16x128_f8f6f4 v[136:139], v[16:23], v[218:225], v[136:139]
	v_mfma_f32_16x16x128_f8f6f4 v[120:123], v[16:23], v[226:233], v[120:123]
	v_mfma_f32_16x16x128_f8f6f4 v[112:115], v[24:31], v[226:233], v[112:115]
	v_mfma_f32_16x16x128_f8f6f4 v[96:99], v[24:31], v[234:241], v[96:99]
	v_mfma_f32_16x16x128_f8f6f4 v[104:107], v[16:23], v[234:241], v[104:107]
	s_barrier
	s_add_i32 s99, s44, 0x17f80
	s_mov_b32 m0, s99
	ds_read_b128 v[210:213], v201 offset:49152
	ds_read_b128 v[218:221], v201 offset:51200
	ds_read_b128 v[214:217], v202 offset:49152
	ds_read_b128 v[222:225], v202 offset:51200
	ds_read_b128 v[226:229], v201 offset:53248
	ds_read_b128 v[234:237], v201 offset:55296
	ds_read_b128 v[230:233], v202 offset:53248
	ds_read_b128 v[238:241], v202 offset:55296
	global_load_lds_dwordx4 v160, s[38:39] offset:128
	s_add_i32 m0, s99, 0x2000
	s_add_i32 s99, s44, 0x1bf80
	global_load_lds_dwordx4 v162, s[38:39] offset:128
	s_mov_b32 m0, s99
	s_nop 0
	global_load_lds_dwordx4 v160, s[40:41] offset:128
	s_add_i32 m0, s99, 0x2000
	s_nop 0
	global_load_lds_dwordx4 v162, s[40:41] offset:128
	s_waitcnt vmcnt(6)
	s_waitcnt lgkmcnt(0)
	s_barrier
	s_waitcnt lgkmcnt(0)
	v_mfma_f32_16x16x128_f8f6f4 v[92:95], v[0:7], v[210:217], v[92:95]
	v_mfma_f32_16x16x128_f8f6f4 v[84:87], v[8:15], v[210:217], v[84:87]
	v_mfma_f32_16x16x128_f8f6f4 v[68:71], v[8:15], v[218:225], v[68:71]
	v_mfma_f32_16x16x128_f8f6f4 v[76:79], v[0:7], v[218:225], v[76:79]
	s_add_i32 m0, s65, 0xffffff80
	v_mfma_f32_16x16x128_f8f6f4 v[60:63], v[0:7], v[226:233], v[60:63]
	global_load_lds_dwordx4 v164, s[36:37] offset:128
	v_mfma_f32_16x16x128_f8f6f4 v[52:55], v[8:15], v[226:233], v[52:55]
	v_mfma_f32_16x16x128_f8f6f4 v[36:39], v[8:15], v[234:241], v[36:39]
	v_mfma_f32_16x16x128_f8f6f4 v[44:47], v[0:7], v[234:241], v[44:47]
	v_mfma_f32_16x16x128_f8f6f4 v[88:91], v[16:23], v[210:217], v[88:91]
	s_add_i32 m0, s66, 0xffffff80
	v_mfma_f32_16x16x128_f8f6f4 v[80:83], v[24:31], v[210:217], v[80:83]
	global_load_lds_dwordx4 v166, s[36:37] offset:128
	v_mfma_f32_16x16x128_f8f6f4 v[64:67], v[24:31], v[218:225], v[64:67]
	v_mfma_f32_16x16x128_f8f6f4 v[72:75], v[16:23], v[218:225], v[72:75]
	v_mfma_f32_16x16x128_f8f6f4 v[56:59], v[16:23], v[226:233], v[56:59]
	v_mfma_f32_16x16x128_f8f6f4 v[48:51], v[24:31], v[226:233], v[48:51]
	v_mfma_f32_16x16x128_f8f6f4 v[32:35], v[24:31], v[234:241], v[32:35]
	v_mfma_f32_16x16x128_f8f6f4 v[40:43], v[16:23], v[234:241], v[40:43]
	s_barrier
	s_add_i32 s89, s89, 2
	s_add_u32 s4, s4, 0x100
	s_addc_u32 s5, s5, 0
	s_cmp_gt_u32 s89, 5
	s_cbranch_scc1 .LBB0_593

.LBB0_672:
	s_add_u32 s36, s6, s34
	s_addc_u32 s37, s7, s35
	s_add_u32 s38, s36, 0x12c00100
	s_addc_u32 s39, s37, 0
	ds_read_b128 v[24:27], v252
	ds_read_b128 v[28:31], v253
	s_and_b64 s[36:37], s[40:41], exec
	ds_read_b128 v[16:19], v252 offset:2048
	ds_read_b128 v[20:23], v253 offset:2048
	s_cselect_b32 s37, s9, s39
	s_cselect_b32 s36, s8, s38
	s_add_u32 s86, s27, s34
	ds_read_b128 v[8:11], v252 offset:16384
	ds_read_b128 v[12:15], v253 offset:16384
	s_addc_u32 s87, s82, s35
	ds_read_b128 v[0:3], v252 offset:18432
	ds_read_b128 v[4:7], v253 offset:18432
	s_and_b64 s[38:39], s[40:41], exec
	s_cselect_b32 s39, s29, s87
	s_cselect_b32 s38, s28, s86
	s_add_u32 s86, s83, s34
	s_addc_u32 s87, s84, s35
	s_and_b64 s[40:41], s[40:41], exec
	s_cselect_b32 s41, s31, s87
	s_cselect_b32 s40, s30, s86
	s_add_u32 s100, s16, s34
	s_addc_u32 s101, s17, s35
	s_add_i32 m0, s59, 0xc000
	ds_read_b128 v[186:189], v207
	ds_read_b128 v[216:219], v207 offset:2048
	ds_read_b128 v[190:193], v208
	ds_read_b128 v[220:223], v208 offset:2048
	ds_read_b128 v[224:227], v207 offset:4096
	ds_read_b128 v[232:235], v207 offset:6144
	ds_read_b128 v[228:231], v208 offset:4096
	ds_read_b128 v[236:239], v208 offset:6144
	global_load_lds_dwordx4 v166, s[100:101]
	s_add_i32 m0, s59, 0xe000
	s_nop 0
	global_load_lds_dwordx4 v168, s[100:101]
	s_waitcnt vmcnt(8)
	s_waitcnt lgkmcnt(0)
	s_barrier
	s_waitcnt lgkmcnt(0)
	v_mfma_f32_16x16x128_f8f6f4 v[156:159], v[24:31], v[186:193], v[156:159]
	v_mfma_f32_16x16x128_f8f6f4 v[152:155], v[16:23], v[186:193], v[152:155]
	v_mfma_f32_16x16x128_f8f6f4 v[136:139], v[16:23], v[216:223], v[136:139]
	v_mfma_f32_16x16x128_f8f6f4 v[140:143], v[24:31], v[216:223], v[140:143]
	v_mfma_f32_16x16x128_f8f6f4 v[124:127], v[24:31], v[224:231], v[124:127]
	v_mfma_f32_16x16x128_f8f6f4 v[120:123], v[16:23], v[224:231], v[120:123]
	v_mfma_f32_16x16x128_f8f6f4 v[104:107], v[16:23], v[232:239], v[104:107]
	v_mfma_f32_16x16x128_f8f6f4 v[108:111], v[24:31], v[232:239], v[108:111]
	v_mfma_f32_16x16x128_f8f6f4 v[148:151], v[8:15], v[186:193], v[148:151]
	v_mfma_f32_16x16x128_f8f6f4 v[144:147], v[0:7], v[186:193], v[144:147]
	v_mfma_f32_16x16x128_f8f6f4 v[128:131], v[0:7], v[216:223], v[128:131]
	v_mfma_f32_16x16x128_f8f6f4 v[132:135], v[8:15], v[216:223], v[132:135]
	v_mfma_f32_16x16x128_f8f6f4 v[116:119], v[8:15], v[224:231], v[116:119]
	v_mfma_f32_16x16x128_f8f6f4 v[112:115], v[0:7], v[224:231], v[112:115]
	v_mfma_f32_16x16x128_f8f6f4 v[96:99], v[0:7], v[232:239], v[96:99]
	v_mfma_f32_16x16x128_f8f6f4 v[100:103], v[8:15], v[232:239], v[100:103]
	s_barrier
	s_add_i32 s86, s69, s42
	s_mov_b32 m0, s86
	ds_read_b128 v[216:219], v207 offset:16384
	ds_read_b128 v[224:227], v207 offset:18432
	ds_read_b128 v[220:223], v208 offset:16384
	ds_read_b128 v[228:231], v208 offset:18432
	ds_read_b128 v[232:235], v207 offset:20480
	ds_read_b128 v[240:243], v207 offset:22528
	ds_read_b128 v[236:239], v208 offset:20480
	ds_read_b128 v[244:247], v208 offset:22528
	global_load_lds_dwordx4 v160, s[38:39]
	s_add_i32 m0, s86, 0x2000
	s_add_i32 s98, s71, s42
	global_load_lds_dwordx4 v162, s[38:39]
	s_mov_b32 m0, s98
	s_nop 0
	global_load_lds_dwordx4 v160, s[40:41]
	s_add_i32 m0, s98, 0x2000
	v_mov_b32_e32 v173, v165
	global_load_lds_dwordx4 v162, s[40:41]
	s_waitcnt vmcnt(6)
	s_waitcnt lgkmcnt(0)
	s_barrier
	s_waitcnt lgkmcnt(0)
	v_mfma_f32_16x16x128_f8f6f4 v[92:95], v[24:31], v[216:223], v[92:95]
	v_mfma_f32_16x16x128_f8f6f4 v[88:91], v[16:23], v[216:223], v[88:91]
	v_mfma_f32_16x16x128_f8f6f4 v[72:75], v[16:23], v[224:231], v[72:75]
	v_mfma_f32_16x16x128_f8f6f4 v[76:79], v[24:31], v[224:231], v[76:79]
	s_mov_b32 m0, s59
	v_mfma_f32_16x16x128_f8f6f4 v[60:63], v[24:31], v[232:239], v[60:63]
	global_load_lds_dwordx4 v164, s[36:37]
	v_mfma_f32_16x16x128_f8f6f4 v[56:59], v[16:23], v[232:239], v[56:59]
	v_mfma_f32_16x16x128_f8f6f4 v[40:43], v[16:23], v[240:247], v[40:43]
	v_mfma_f32_16x16x128_f8f6f4 v[44:47], v[24:31], v[240:247], v[44:47]
	v_mfma_f32_16x16x128_f8f6f4 v[84:87], v[8:15], v[216:223], v[84:87]
	s_mov_b32 m0, s60
	v_mfma_f32_16x16x128_f8f6f4 v[80:83], v[0:7], v[216:223], v[80:83]
	global_load_lds_dwordx4 v172, s[36:37]
	v_mfma_f32_16x16x128_f8f6f4 v[64:67], v[0:7], v[224:231], v[64:67]
	v_mfma_f32_16x16x128_f8f6f4 v[68:71], v[8:15], v[224:231], v[68:71]
	v_mfma_f32_16x16x128_f8f6f4 v[52:55], v[8:15], v[232:239], v[52:55]
	v_mfma_f32_16x16x128_f8f6f4 v[48:51], v[0:7], v[232:239], v[48:51]
	v_mfma_f32_16x16x128_f8f6f4 v[32:35], v[0:7], v[240:247], v[32:35]
	v_mfma_f32_16x16x128_f8f6f4 v[36:39], v[8:15], v[240:247], v[36:39]
	s_barrier
	ds_read_b128 v[0:3], v252 offset:32768
	ds_read_b128 v[4:7], v253 offset:32768
	ds_read_b128 v[8:11], v252 offset:34816
	ds_read_b128 v[12:15], v253 offset:34816
	ds_read_b128 v[16:19], v252 offset:49152
	ds_read_b128 v[20:23], v253 offset:49152
	ds_read_b128 v[24:27], v252 offset:51200
	ds_read_b128 v[28:31], v253 offset:51200
	s_mov_b32 m0, s61
	ds_read_b128 v[216:219], v207 offset:32768
	ds_read_b128 v[224:227], v207 offset:34816
	ds_read_b128 v[220:223], v208 offset:32768
	ds_read_b128 v[228:231], v208 offset:34816
	ds_read_b128 v[232:235], v207 offset:36864
	ds_read_b128 v[240:243], v207 offset:38912
	ds_read_b128 v[236:239], v208 offset:36864
	ds_read_b128 v[244:247], v208 offset:38912
	global_load_lds_dwordx4 v184, s[36:37]
	s_mov_b32 m0, s62
	s_nop 0
	global_load_lds_dwordx4 v182, s[36:37]
	s_waitcnt vmcnt(8)
	s_waitcnt lgkmcnt(0)
	s_barrier
	s_waitcnt lgkmcnt(0)
	v_mfma_f32_16x16x128_f8f6f4 v[156:159], v[0:7], v[216:223], v[156:159]
	v_mfma_f32_16x16x128_f8f6f4 v[152:155], v[8:15], v[216:223], v[152:155]
	v_mfma_f32_16x16x128_f8f6f4 v[136:139], v[8:15], v[224:231], v[136:139]
	v_mfma_f32_16x16x128_f8f6f4 v[140:143], v[0:7], v[224:231], v[140:143]
	v_mfma_f32_16x16x128_f8f6f4 v[124:127], v[0:7], v[232:239], v[124:127]
	v_mfma_f32_16x16x128_f8f6f4 v[120:123], v[8:15], v[232:239], v[120:123]
	v_mfma_f32_16x16x128_f8f6f4 v[104:107], v[8:15], v[240:247], v[104:107]
	v_mfma_f32_16x16x128_f8f6f4 v[108:111], v[0:7], v[240:247], v[108:111]
	v_mfma_f32_16x16x128_f8f6f4 v[148:151], v[16:23], v[216:223], v[148:151]
	v_mfma_f32_16x16x128_f8f6f4 v[144:147], v[24:31], v[216:223], v[144:147]
	v_mfma_f32_16x16x128_f8f6f4 v[128:131], v[24:31], v[224:231], v[128:131]
	v_mfma_f32_16x16x128_f8f6f4 v[132:135], v[16:23], v[224:231], v[132:135]
	v_mfma_f32_16x16x128_f8f6f4 v[116:119], v[16:23], v[232:239], v[116:119]
	v_mfma_f32_16x16x128_f8f6f4 v[112:115], v[24:31], v[232:239], v[112:115]
	v_mfma_f32_16x16x128_f8f6f4 v[96:99], v[24:31], v[240:247], v[96:99]
	v_mfma_f32_16x16x128_f8f6f4 v[100:103], v[16:23], v[240:247], v[100:103]
	s_barrier
	s_add_i32 s99, s42, 0x17f80
	s_mov_b32 m0, s99
	ds_read_b128 v[216:219], v207 offset:49152
	ds_read_b128 v[224:227], v207 offset:51200
	ds_read_b128 v[220:223], v208 offset:49152
	ds_read_b128 v[228:231], v208 offset:51200
	ds_read_b128 v[232:235], v207 offset:53248
	ds_read_b128 v[240:243], v207 offset:55296
	ds_read_b128 v[236:239], v208 offset:53248
	ds_read_b128 v[244:247], v208 offset:55296
	global_load_lds_dwordx4 v160, s[38:39] offset:128
	s_add_i32 m0, s99, 0x2000
	s_add_i32 s99, s42, 0x1bf80
	global_load_lds_dwordx4 v162, s[38:39] offset:128
	s_mov_b32 m0, s99
	s_nop 0
	global_load_lds_dwordx4 v160, s[40:41] offset:128
	s_add_i32 m0, s99, 0x2000
	s_nop 0
	global_load_lds_dwordx4 v162, s[40:41] offset:128
	s_waitcnt vmcnt(6)
	s_waitcnt lgkmcnt(0)
	s_barrier
	s_waitcnt lgkmcnt(0)
	v_mfma_f32_16x16x128_f8f6f4 v[92:95], v[0:7], v[216:223], v[92:95]
	v_mfma_f32_16x16x128_f8f6f4 v[88:91], v[8:15], v[216:223], v[88:91]
	v_mfma_f32_16x16x128_f8f6f4 v[72:75], v[8:15], v[224:231], v[72:75]
	v_mfma_f32_16x16x128_f8f6f4 v[76:79], v[0:7], v[224:231], v[76:79]
	s_add_i32 m0, s63, 0xffffff80
	v_mfma_f32_16x16x128_f8f6f4 v[60:63], v[0:7], v[232:239], v[60:63]
	global_load_lds_dwordx4 v164, s[36:37] offset:128
	v_mfma_f32_16x16x128_f8f6f4 v[56:59], v[8:15], v[232:239], v[56:59]
	v_mfma_f32_16x16x128_f8f6f4 v[40:43], v[8:15], v[240:247], v[40:43]
	v_mfma_f32_16x16x128_f8f6f4 v[44:47], v[0:7], v[240:247], v[44:47]
	v_mfma_f32_16x16x128_f8f6f4 v[84:87], v[16:23], v[216:223], v[84:87]
	s_add_i32 m0, s64, 0xffffff80
	v_mfma_f32_16x16x128_f8f6f4 v[80:83], v[24:31], v[216:223], v[80:83]
	global_load_lds_dwordx4 v172, s[36:37] offset:128
	v_mfma_f32_16x16x128_f8f6f4 v[64:67], v[24:31], v[224:231], v[64:67]
	v_mfma_f32_16x16x128_f8f6f4 v[68:71], v[16:23], v[224:231], v[68:71]
	v_mfma_f32_16x16x128_f8f6f4 v[52:55], v[16:23], v[232:239], v[52:55]
	v_mfma_f32_16x16x128_f8f6f4 v[48:51], v[24:31], v[232:239], v[48:51]
	v_mfma_f32_16x16x128_f8f6f4 v[32:35], v[24:31], v[240:247], v[32:35]
	v_mfma_f32_16x16x128_f8f6f4 v[36:39], v[16:23], v[240:247], v[36:39]
	s_barrier
	s_add_i32 s85, s85, 2
	s_add_u32 s34, s34, 0x100
	s_addc_u32 s35, s35, 0
	s_cmp_gt_u32 s85, 5
	s_cbranch_scc1 .LBB0_675

.LBB0_817:
	s_add_u32 s28, s10, s26
	s_addc_u32 s29, s11, s27
	s_add_u32 s30, s28, 0x38000100
	s_addc_u32 s31, s29, 0
	ds_read_b128 v[24:27], v252
	ds_read_b128 v[28:31], v253
	s_and_b64 s[28:29], s[34:35], exec
	ds_read_b128 v[16:19], v252 offset:2048
	ds_read_b128 v[20:23], v253 offset:2048
	s_cselect_b32 s29, s1, s31
	s_cselect_b32 s28, s0, s30
	s_add_u32 s61, s56, s26
	ds_read_b128 v[8:11], v252 offset:16384
	ds_read_b128 v[12:15], v253 offset:16384
	s_addc_u32 s62, s57, s27
	ds_read_b128 v[0:3], v252 offset:18432
	ds_read_b128 v[4:7], v253 offset:18432
	s_and_b64 s[30:31], s[34:35], exec
	s_cselect_b32 s31, s23, s62
	s_cselect_b32 s30, s22, s61
	s_add_u32 s61, s58, s26
	s_addc_u32 s62, s59, s27
	s_and_b64 s[34:35], s[34:35], exec
	s_cselect_b32 s35, s25, s62
	s_cselect_b32 s34, s24, s61
	s_add_u32 s100, s14, s26
	s_addc_u32 s101, s15, s27
	s_add_i32 m0, s37, 0xc000
	ds_read_b128 v[186:189], v207
	ds_read_b128 v[216:219], v207 offset:2048
	ds_read_b128 v[190:193], v208
	ds_read_b128 v[220:223], v208 offset:2048
	ds_read_b128 v[224:227], v207 offset:4096
	ds_read_b128 v[232:235], v207 offset:6144
	ds_read_b128 v[228:231], v208 offset:4096
	ds_read_b128 v[236:239], v208 offset:6144
	global_load_lds_dwordx4 v168, s[100:101]
	s_add_i32 m0, s37, 0xe000
	s_nop 0
	global_load_lds_dwordx4 v170, s[100:101]
	s_waitcnt vmcnt(8)
	s_waitcnt lgkmcnt(0)
	s_barrier
	s_waitcnt lgkmcnt(0)
	v_mfma_f32_16x16x128_f8f6f4 v[156:159], v[24:31], v[186:193], v[156:159]
	v_mfma_f32_16x16x128_f8f6f4 v[152:155], v[16:23], v[186:193], v[152:155]
	v_mfma_f32_16x16x128_f8f6f4 v[136:139], v[16:23], v[216:223], v[136:139]
	v_mfma_f32_16x16x128_f8f6f4 v[140:143], v[24:31], v[216:223], v[140:143]
	v_mfma_f32_16x16x128_f8f6f4 v[124:127], v[24:31], v[224:231], v[124:127]
	v_mfma_f32_16x16x128_f8f6f4 v[120:123], v[16:23], v[224:231], v[120:123]
	v_mfma_f32_16x16x128_f8f6f4 v[104:107], v[16:23], v[232:239], v[104:107]
	v_mfma_f32_16x16x128_f8f6f4 v[108:111], v[24:31], v[232:239], v[108:111]
	v_mfma_f32_16x16x128_f8f6f4 v[148:151], v[8:15], v[186:193], v[148:151]
	v_mfma_f32_16x16x128_f8f6f4 v[144:147], v[0:7], v[186:193], v[144:147]
	v_mfma_f32_16x16x128_f8f6f4 v[128:131], v[0:7], v[216:223], v[128:131]
	v_mfma_f32_16x16x128_f8f6f4 v[132:135], v[8:15], v[216:223], v[132:135]
	v_mfma_f32_16x16x128_f8f6f4 v[116:119], v[8:15], v[224:231], v[116:119]
	v_mfma_f32_16x16x128_f8f6f4 v[112:115], v[0:7], v[224:231], v[112:115]
	v_mfma_f32_16x16x128_f8f6f4 v[96:99], v[0:7], v[232:239], v[96:99]
	v_mfma_f32_16x16x128_f8f6f4 v[100:103], v[8:15], v[232:239], v[100:103]
	s_barrier
	s_add_i32 s61, s44, s36
	s_mov_b32 m0, s61
	ds_read_b128 v[216:219], v207 offset:16384
	ds_read_b128 v[224:227], v207 offset:18432
	ds_read_b128 v[220:223], v208 offset:16384
	ds_read_b128 v[228:231], v208 offset:18432
	ds_read_b128 v[232:235], v207 offset:20480
	ds_read_b128 v[240:243], v207 offset:22528
	ds_read_b128 v[236:239], v208 offset:20480
	ds_read_b128 v[244:247], v208 offset:22528
	global_load_lds_dwordx4 v160, s[30:31]
	s_add_i32 m0, s61, 0x2000
	s_add_i32 s98, s46, s36
	global_load_lds_dwordx4 v162, s[30:31]
	s_mov_b32 m0, s98
	s_nop 0
	global_load_lds_dwordx4 v160, s[34:35]
	s_add_i32 m0, s98, 0x2000
	v_mov_b32_e32 v167, v165
	global_load_lds_dwordx4 v162, s[34:35]
	s_waitcnt vmcnt(6)
	s_waitcnt lgkmcnt(0)
	s_barrier
	s_waitcnt lgkmcnt(0)
	v_mfma_f32_16x16x128_f8f6f4 v[92:95], v[24:31], v[216:223], v[92:95]
	v_mfma_f32_16x16x128_f8f6f4 v[88:91], v[16:23], v[216:223], v[88:91]
	v_mfma_f32_16x16x128_f8f6f4 v[72:75], v[16:23], v[224:231], v[72:75]
	v_mfma_f32_16x16x128_f8f6f4 v[76:79], v[24:31], v[224:231], v[76:79]
	s_mov_b32 m0, s37
	v_mfma_f32_16x16x128_f8f6f4 v[60:63], v[24:31], v[232:239], v[60:63]
	global_load_lds_dwordx4 v164, s[28:29]
	v_mfma_f32_16x16x128_f8f6f4 v[56:59], v[16:23], v[232:239], v[56:59]
	v_mfma_f32_16x16x128_f8f6f4 v[40:43], v[16:23], v[240:247], v[40:43]
	v_mfma_f32_16x16x128_f8f6f4 v[44:47], v[24:31], v[240:247], v[44:47]
	v_mfma_f32_16x16x128_f8f6f4 v[84:87], v[8:15], v[216:223], v[84:87]
	s_mov_b32 m0, s38
	v_mfma_f32_16x16x128_f8f6f4 v[80:83], v[0:7], v[216:223], v[80:83]
	global_load_lds_dwordx4 v166, s[28:29]
	v_mfma_f32_16x16x128_f8f6f4 v[64:67], v[0:7], v[224:231], v[64:67]
	v_mfma_f32_16x16x128_f8f6f4 v[68:71], v[8:15], v[224:231], v[68:71]
	v_mfma_f32_16x16x128_f8f6f4 v[52:55], v[8:15], v[232:239], v[52:55]
	v_mfma_f32_16x16x128_f8f6f4 v[48:51], v[0:7], v[232:239], v[48:51]
	v_mfma_f32_16x16x128_f8f6f4 v[32:35], v[0:7], v[240:247], v[32:35]
	v_mfma_f32_16x16x128_f8f6f4 v[36:39], v[8:15], v[240:247], v[36:39]
	s_barrier
	ds_read_b128 v[0:3], v252 offset:32768
	ds_read_b128 v[4:7], v253 offset:32768
	ds_read_b128 v[8:11], v252 offset:34816
	ds_read_b128 v[12:15], v253 offset:34816
	ds_read_b128 v[16:19], v252 offset:49152
	ds_read_b128 v[20:23], v253 offset:49152
	ds_read_b128 v[24:27], v252 offset:51200
	ds_read_b128 v[28:31], v253 offset:51200
	s_mov_b32 m0, s39
	ds_read_b128 v[216:219], v207 offset:32768
	ds_read_b128 v[224:227], v207 offset:34816
	ds_read_b128 v[220:223], v208 offset:32768
	ds_read_b128 v[228:231], v208 offset:34816
	ds_read_b128 v[232:235], v207 offset:36864
	ds_read_b128 v[240:243], v207 offset:38912
	ds_read_b128 v[236:239], v208 offset:36864
	ds_read_b128 v[244:247], v208 offset:38912
	global_load_lds_dwordx4 v184, s[28:29]
	s_mov_b32 m0, s40
	s_nop 0
	global_load_lds_dwordx4 v182, s[28:29]
	s_waitcnt vmcnt(8)
	s_waitcnt lgkmcnt(0)
	s_barrier
	s_waitcnt lgkmcnt(0)
	v_mfma_f32_16x16x128_f8f6f4 v[156:159], v[0:7], v[216:223], v[156:159]
	v_mfma_f32_16x16x128_f8f6f4 v[152:155], v[8:15], v[216:223], v[152:155]
	v_mfma_f32_16x16x128_f8f6f4 v[136:139], v[8:15], v[224:231], v[136:139]
	v_mfma_f32_16x16x128_f8f6f4 v[140:143], v[0:7], v[224:231], v[140:143]
	v_mfma_f32_16x16x128_f8f6f4 v[124:127], v[0:7], v[232:239], v[124:127]
	v_mfma_f32_16x16x128_f8f6f4 v[120:123], v[8:15], v[232:239], v[120:123]
	v_mfma_f32_16x16x128_f8f6f4 v[104:107], v[8:15], v[240:247], v[104:107]
	v_mfma_f32_16x16x128_f8f6f4 v[108:111], v[0:7], v[240:247], v[108:111]
	v_mfma_f32_16x16x128_f8f6f4 v[148:151], v[16:23], v[216:223], v[148:151]
	v_mfma_f32_16x16x128_f8f6f4 v[144:147], v[24:31], v[216:223], v[144:147]
	v_mfma_f32_16x16x128_f8f6f4 v[128:131], v[24:31], v[224:231], v[128:131]
	v_mfma_f32_16x16x128_f8f6f4 v[132:135], v[16:23], v[224:231], v[132:135]
	v_mfma_f32_16x16x128_f8f6f4 v[116:119], v[16:23], v[232:239], v[116:119]
	v_mfma_f32_16x16x128_f8f6f4 v[112:115], v[24:31], v[232:239], v[112:115]
	v_mfma_f32_16x16x128_f8f6f4 v[96:99], v[24:31], v[240:247], v[96:99]
	v_mfma_f32_16x16x128_f8f6f4 v[100:103], v[16:23], v[240:247], v[100:103]
	s_barrier
	s_add_i32 s99, s36, 0x17f80
	s_mov_b32 m0, s99
	ds_read_b128 v[216:219], v207 offset:49152
	ds_read_b128 v[224:227], v207 offset:51200
	ds_read_b128 v[220:223], v208 offset:49152
	ds_read_b128 v[228:231], v208 offset:51200
	ds_read_b128 v[232:235], v207 offset:53248
	ds_read_b128 v[240:243], v207 offset:55296
	ds_read_b128 v[236:239], v208 offset:53248
	ds_read_b128 v[244:247], v208 offset:55296
	global_load_lds_dwordx4 v160, s[30:31] offset:128
	s_add_i32 m0, s99, 0x2000
	s_add_i32 s99, s36, 0x1bf80
	global_load_lds_dwordx4 v162, s[30:31] offset:128
	s_mov_b32 m0, s99
	s_nop 0
	global_load_lds_dwordx4 v160, s[34:35] offset:128
	s_add_i32 m0, s99, 0x2000
	s_nop 0
	global_load_lds_dwordx4 v162, s[34:35] offset:128
	s_waitcnt vmcnt(6)
	s_waitcnt lgkmcnt(0)
	s_barrier
	s_waitcnt lgkmcnt(0)
	v_mfma_f32_16x16x128_f8f6f4 v[92:95], v[0:7], v[216:223], v[92:95]
	v_mfma_f32_16x16x128_f8f6f4 v[88:91], v[8:15], v[216:223], v[88:91]
	v_mfma_f32_16x16x128_f8f6f4 v[72:75], v[8:15], v[224:231], v[72:75]
	v_mfma_f32_16x16x128_f8f6f4 v[76:79], v[0:7], v[224:231], v[76:79]
	s_add_i32 m0, s41, 0xffffff80
	v_mfma_f32_16x16x128_f8f6f4 v[60:63], v[0:7], v[232:239], v[60:63]
	global_load_lds_dwordx4 v164, s[28:29] offset:128
	v_mfma_f32_16x16x128_f8f6f4 v[56:59], v[8:15], v[232:239], v[56:59]
	v_mfma_f32_16x16x128_f8f6f4 v[40:43], v[8:15], v[240:247], v[40:43]
	v_mfma_f32_16x16x128_f8f6f4 v[44:47], v[0:7], v[240:247], v[44:47]
	v_mfma_f32_16x16x128_f8f6f4 v[84:87], v[16:23], v[216:223], v[84:87]
	s_add_i32 m0, s42, 0xffffff80
	v_mfma_f32_16x16x128_f8f6f4 v[80:83], v[24:31], v[216:223], v[80:83]
	global_load_lds_dwordx4 v166, s[28:29] offset:128
	v_mfma_f32_16x16x128_f8f6f4 v[64:67], v[24:31], v[224:231], v[64:67]
	v_mfma_f32_16x16x128_f8f6f4 v[68:71], v[16:23], v[224:231], v[68:71]
	v_mfma_f32_16x16x128_f8f6f4 v[52:55], v[16:23], v[232:239], v[52:55]
	v_mfma_f32_16x16x128_f8f6f4 v[48:51], v[24:31], v[232:239], v[48:51]
	v_mfma_f32_16x16x128_f8f6f4 v[32:35], v[24:31], v[240:247], v[32:35]
	v_mfma_f32_16x16x128_f8f6f4 v[36:39], v[16:23], v[240:247], v[36:39]
	s_barrier
	s_add_i32 s60, s60, 2
	s_add_u32 s26, s26, 0x100
	s_addc_u32 s27, s27, 0
	s_cmp_gt_u32 s60, 5
	s_cbranch_scc1 .LBB0_820

.LBB0_839:
	s_add_u32 s6, s10, s4
	s_addc_u32 s7, s11, s5
	s_add_u32 s34, s6, 0xe000100
	s_addc_u32 s35, s7, 0
	ds_read_b128 v[166:169], v252
	ds_read_b128 v[170:173], v253
	s_and_b64 s[6:7], s[30:31], exec
	ds_read_b128 v[174:177], v252 offset:2048
	ds_read_b128 v[178:181], v253 offset:2048
	s_cselect_b32 s7, s1, s35
	s_cselect_b32 s6, s0, s34
	s_add_u32 s62, s36, s4
	ds_read_b128 v[182:185], v252 offset:16384
	ds_read_b128 v[186:189], v253 offset:16384
	s_addc_u32 s63, s37, s5
	ds_read_b128 v[190:193], v252 offset:18432
	ds_read_b128 v[194:197], v253 offset:18432
	s_and_b64 s[34:35], s[30:31], exec
	s_cselect_b32 s35, s27, s63
	s_cselect_b32 s34, s26, s62
	s_add_u32 s62, s57, s4
	s_addc_u32 s63, s60, s5
	s_and_b64 s[30:31], s[30:31], exec
	s_cselect_b32 s31, s29, s63
	s_cselect_b32 s30, s28, s62
	v_lshl_add_u64 v[232:233], v[148:149], 0, s[4:5]
	s_add_i32 m0, s40, 0xc000
	ds_read_b128 v[200:203], v161
	ds_read_b128 v[204:207], v161 offset:1024
	ds_read_b128 v[208:211], v161 offset:2048
	ds_read_b128 v[212:215], v161 offset:3072
	ds_read_b128 v[216:219], v161 offset:4096
	ds_read_b128 v[220:223], v161 offset:5120
	ds_read_b128 v[224:227], v161 offset:6144
	ds_read_b128 v[228:231], v161 offset:7168
	global_load_lds_dwordx4 v[232:233], off
	v_lshl_add_u64 v[232:233], v[146:147], 0, s[4:5]
	s_add_i32 m0, s40, 0xe000
	s_nop 0
	global_load_lds_dwordx4 v[232:233], off
	s_waitcnt vmcnt(8)
	s_waitcnt lgkmcnt(0)
	s_barrier
	s_waitcnt lgkmcnt(0)
	v_mfma_f32_16x16x32_bf16 v[124:127], v[166:169], v[200:203], v[124:127]
	v_mfma_f32_16x16x32_bf16 v[120:123], v[174:177], v[200:203], v[120:123]
	v_mfma_f32_16x16x32_bf16 v[108:111], v[166:169], v[208:211], v[108:111]
	v_mfma_f32_16x16x32_bf16 v[104:107], v[174:177], v[208:211], v[104:107]
	v_mfma_f32_16x16x32_bf16 v[92:95], v[166:169], v[216:219], v[92:95]
	v_mfma_f32_16x16x32_bf16 v[88:91], v[174:177], v[216:219], v[88:91]
	v_mfma_f32_16x16x32_bf16 v[76:79], v[166:169], v[224:227], v[76:79]
	v_mfma_f32_16x16x32_bf16 v[72:75], v[174:177], v[224:227], v[72:75]
	v_mfma_f32_16x16x32_bf16 v[124:127], v[170:173], v[204:207], v[124:127]
	v_mfma_f32_16x16x32_bf16 v[120:123], v[178:181], v[204:207], v[120:123]
	v_mfma_f32_16x16x32_bf16 v[108:111], v[170:173], v[212:215], v[108:111]
	v_mfma_f32_16x16x32_bf16 v[104:107], v[178:181], v[212:215], v[104:107]
	v_mfma_f32_16x16x32_bf16 v[92:95], v[170:173], v[220:223], v[92:95]
	v_mfma_f32_16x16x32_bf16 v[88:91], v[178:181], v[220:223], v[88:91]
	v_mfma_f32_16x16x32_bf16 v[76:79], v[170:173], v[228:231], v[76:79]
	v_mfma_f32_16x16x32_bf16 v[72:75], v[178:181], v[228:231], v[72:75]
	v_mfma_f32_16x16x32_bf16 v[116:119], v[182:185], v[200:203], v[116:119]
	v_mfma_f32_16x16x32_bf16 v[112:115], v[190:193], v[200:203], v[112:115]
	v_mfma_f32_16x16x32_bf16 v[100:103], v[182:185], v[208:211], v[100:103]
	v_mfma_f32_16x16x32_bf16 v[96:99], v[190:193], v[208:211], v[96:99]
	v_mfma_f32_16x16x32_bf16 v[84:87], v[182:185], v[216:219], v[84:87]
	v_mfma_f32_16x16x32_bf16 v[80:83], v[190:193], v[216:219], v[80:83]
	v_mfma_f32_16x16x32_bf16 v[68:71], v[182:185], v[224:227], v[68:71]
	v_mfma_f32_16x16x32_bf16 v[64:67], v[190:193], v[224:227], v[64:67]
	v_mfma_f32_16x16x32_bf16 v[116:119], v[186:189], v[204:207], v[116:119]
	v_mfma_f32_16x16x32_bf16 v[112:115], v[194:197], v[204:207], v[112:115]
	v_mfma_f32_16x16x32_bf16 v[100:103], v[186:189], v[212:215], v[100:103]
	v_mfma_f32_16x16x32_bf16 v[96:99], v[194:197], v[212:215], v[96:99]
	v_mfma_f32_16x16x32_bf16 v[84:87], v[186:189], v[220:223], v[84:87]
	v_mfma_f32_16x16x32_bf16 v[80:83], v[194:197], v[220:223], v[80:83]
	v_mfma_f32_16x16x32_bf16 v[68:71], v[186:189], v[228:231], v[68:71]
	v_mfma_f32_16x16x32_bf16 v[64:67], v[194:197], v[228:231], v[64:67]
	s_barrier
	s_add_i32 s62, s49, s39
	v_lshl_add_u64 v[232:233], s[34:35], 0, v[132:133]
	s_mov_b32 m0, s62
	ds_read_b128 v[200:203], v161 offset:16384
	ds_read_b128 v[204:207], v161 offset:17408
	ds_read_b128 v[208:211], v161 offset:18432
	ds_read_b128 v[212:215], v161 offset:19456
	ds_read_b128 v[216:219], v161 offset:20480
	ds_read_b128 v[220:223], v161 offset:21504
	ds_read_b128 v[224:227], v161 offset:22528
	ds_read_b128 v[228:231], v161 offset:23552
	global_load_lds_dwordx4 v[232:233], off
	v_lshl_add_u64 v[234:235], s[34:35], 0, v[134:135]
	s_add_i32 m0, s62, 0x2000
	s_add_i32 s34, s51, s39
	global_load_lds_dwordx4 v[234:235], off
	v_lshl_add_u64 v[236:237], s[30:31], 0, v[132:133]
	s_mov_b32 m0, s34
	v_lshl_add_u64 v[238:239], s[30:31], 0, v[134:135]
	global_load_lds_dwordx4 v[236:237], off
	s_add_i32 m0, s34, 0x2000
	v_mov_b32_e32 v139, v137
	global_load_lds_dwordx4 v[238:239], off
	s_mov_b32 m0, s40
	v_lshl_add_u64 v[240:241], s[6:7], 0, v[136:137]
	global_load_lds_dwordx4 v136, s[6:7]
	s_mov_b32 m0, s41
	v_lshl_add_u64 v[242:243], s[6:7], 0, v[138:139]
	global_load_lds_dwordx4 v138, s[6:7]
	s_waitcnt vmcnt(8)
	s_waitcnt lgkmcnt(0)
	s_barrier
	s_waitcnt lgkmcnt(0)
	v_mfma_f32_16x16x32_bf16 v[60:63], v[166:169], v[200:203], v[60:63]
	v_mfma_f32_16x16x32_bf16 v[56:59], v[174:177], v[200:203], v[56:59]
	v_mfma_f32_16x16x32_bf16 v[44:47], v[166:169], v[208:211], v[44:47]
	v_mfma_f32_16x16x32_bf16 v[40:43], v[174:177], v[208:211], v[40:43]
	v_mfma_f32_16x16x32_bf16 v[28:31], v[166:169], v[216:219], v[28:31]
	v_mfma_f32_16x16x32_bf16 v[24:27], v[174:177], v[216:219], v[24:27]
	v_mfma_f32_16x16x32_bf16 v[12:15], v[166:169], v[224:227], v[12:15]
	v_mfma_f32_16x16x32_bf16 v[8:11], v[174:177], v[224:227], v[8:11]
	v_mfma_f32_16x16x32_bf16 v[60:63], v[170:173], v[204:207], v[60:63]
	v_mfma_f32_16x16x32_bf16 v[56:59], v[178:181], v[204:207], v[56:59]
	v_mfma_f32_16x16x32_bf16 v[44:47], v[170:173], v[212:215], v[44:47]
	v_mfma_f32_16x16x32_bf16 v[40:43], v[178:181], v[212:215], v[40:43]
	v_mfma_f32_16x16x32_bf16 v[28:31], v[170:173], v[220:223], v[28:31]
	v_mfma_f32_16x16x32_bf16 v[24:27], v[178:181], v[220:223], v[24:27]
	v_mfma_f32_16x16x32_bf16 v[12:15], v[170:173], v[228:231], v[12:15]
	v_mfma_f32_16x16x32_bf16 v[8:11], v[178:181], v[228:231], v[8:11]
	v_mfma_f32_16x16x32_bf16 v[52:55], v[182:185], v[200:203], v[52:55]
	v_mfma_f32_16x16x32_bf16 v[48:51], v[190:193], v[200:203], v[48:51]
	v_mfma_f32_16x16x32_bf16 v[36:39], v[182:185], v[208:211], v[36:39]
	v_mfma_f32_16x16x32_bf16 v[32:35], v[190:193], v[208:211], v[32:35]
	v_mfma_f32_16x16x32_bf16 v[20:23], v[182:185], v[216:219], v[20:23]
	v_mfma_f32_16x16x32_bf16 v[16:19], v[190:193], v[216:219], v[16:19]
	v_mfma_f32_16x16x32_bf16 v[4:7], v[182:185], v[224:227], v[4:7]
	v_mfma_f32_16x16x32_bf16 v[0:3], v[190:193], v[224:227], v[0:3]
	v_mfma_f32_16x16x32_bf16 v[52:55], v[186:189], v[204:207], v[52:55]
	v_mfma_f32_16x16x32_bf16 v[48:51], v[194:197], v[204:207], v[48:51]
	v_mfma_f32_16x16x32_bf16 v[36:39], v[186:189], v[212:215], v[36:39]
	v_mfma_f32_16x16x32_bf16 v[32:35], v[194:197], v[212:215], v[32:35]
	v_mfma_f32_16x16x32_bf16 v[20:23], v[186:189], v[220:223], v[20:23]
	v_mfma_f32_16x16x32_bf16 v[16:19], v[194:197], v[220:223], v[16:19]
	v_mfma_f32_16x16x32_bf16 v[4:7], v[186:189], v[228:231], v[4:7]
	v_mfma_f32_16x16x32_bf16 v[0:3], v[194:197], v[228:231], v[0:3]
	s_barrier
	s_add_i32 s30, 0, 0x18000
	ds_read_b128 v[166:169], v252 offset:32768
	ds_read_b128 v[170:173], v253 offset:32768
	s_add_i32 s31, 0, 0x1c000
	ds_read_b128 v[174:177], v252 offset:34816
	ds_read_b128 v[178:181], v253 offset:34816
	ds_read_b128 v[182:185], v252 offset:49152
	ds_read_b128 v[186:189], v253 offset:49152
	ds_read_b128 v[190:193], v252 offset:51200
	ds_read_b128 v[194:197], v253 offset:51200
	s_mov_b32 m0, s42
	v_lshl_add_u64 v[152:153], s[6:7], 0, v[152:153]
	ds_read_b128 v[200:203], v161 offset:32768
	ds_read_b128 v[204:207], v161 offset:33792
	ds_read_b128 v[208:211], v161 offset:34816
	ds_read_b128 v[212:215], v161 offset:35840
	ds_read_b128 v[216:219], v161 offset:36864
	ds_read_b128 v[220:223], v161 offset:37888
	ds_read_b128 v[224:227], v161 offset:38912
	ds_read_b128 v[228:231], v161 offset:39936
	global_load_lds_dwordx4 v[152:153], off
	v_lshl_add_u64 v[150:151], s[6:7], 0, v[150:151]
	s_mov_b32 m0, s43
	s_nop 0
	global_load_lds_dwordx4 v[150:151], off
	s_waitcnt vmcnt(8)
	s_waitcnt lgkmcnt(0)
	s_barrier
	s_waitcnt lgkmcnt(0)
	v_mfma_f32_16x16x32_bf16 v[124:127], v[166:169], v[200:203], v[124:127]
	v_mfma_f32_16x16x32_bf16 v[120:123], v[174:177], v[200:203], v[120:123]
	v_mfma_f32_16x16x32_bf16 v[108:111], v[166:169], v[208:211], v[108:111]
	v_mfma_f32_16x16x32_bf16 v[104:107], v[174:177], v[208:211], v[104:107]
	v_mfma_f32_16x16x32_bf16 v[92:95], v[166:169], v[216:219], v[92:95]
	v_mfma_f32_16x16x32_bf16 v[88:91], v[174:177], v[216:219], v[88:91]
	v_mfma_f32_16x16x32_bf16 v[76:79], v[166:169], v[224:227], v[76:79]
	v_mfma_f32_16x16x32_bf16 v[72:75], v[174:177], v[224:227], v[72:75]
	v_mfma_f32_16x16x32_bf16 v[124:127], v[170:173], v[204:207], v[124:127]
	v_mfma_f32_16x16x32_bf16 v[120:123], v[178:181], v[204:207], v[120:123]
	v_mfma_f32_16x16x32_bf16 v[108:111], v[170:173], v[212:215], v[108:111]
	v_mfma_f32_16x16x32_bf16 v[104:107], v[178:181], v[212:215], v[104:107]
	v_mfma_f32_16x16x32_bf16 v[92:95], v[170:173], v[220:223], v[92:95]
	v_mfma_f32_16x16x32_bf16 v[88:91], v[178:181], v[220:223], v[88:91]
	v_mfma_f32_16x16x32_bf16 v[76:79], v[170:173], v[228:231], v[76:79]
	v_mfma_f32_16x16x32_bf16 v[72:75], v[178:181], v[228:231], v[72:75]
	v_mfma_f32_16x16x32_bf16 v[116:119], v[182:185], v[200:203], v[116:119]
	v_mfma_f32_16x16x32_bf16 v[112:115], v[190:193], v[200:203], v[112:115]
	v_mfma_f32_16x16x32_bf16 v[100:103], v[182:185], v[208:211], v[100:103]
	v_mfma_f32_16x16x32_bf16 v[96:99], v[190:193], v[208:211], v[96:99]
	v_mfma_f32_16x16x32_bf16 v[84:87], v[182:185], v[216:219], v[84:87]
	v_mfma_f32_16x16x32_bf16 v[80:83], v[190:193], v[216:219], v[80:83]
	v_mfma_f32_16x16x32_bf16 v[68:71], v[182:185], v[224:227], v[68:71]
	v_mfma_f32_16x16x32_bf16 v[64:67], v[190:193], v[224:227], v[64:67]
	v_mfma_f32_16x16x32_bf16 v[116:119], v[186:189], v[204:207], v[116:119]
	v_mfma_f32_16x16x32_bf16 v[112:115], v[194:197], v[204:207], v[112:115]
	v_mfma_f32_16x16x32_bf16 v[100:103], v[186:189], v[212:215], v[100:103]
	v_mfma_f32_16x16x32_bf16 v[96:99], v[194:197], v[212:215], v[96:99]
	v_mfma_f32_16x16x32_bf16 v[84:87], v[186:189], v[220:223], v[84:87]
	v_mfma_f32_16x16x32_bf16 v[80:83], v[194:197], v[220:223], v[80:83]
	v_mfma_f32_16x16x32_bf16 v[68:71], v[186:189], v[228:231], v[68:71]
	v_mfma_f32_16x16x32_bf16 v[64:67], v[194:197], v[228:231], v[64:67]
	s_barrier
	s_add_i32 s6, s30, s39
	v_lshl_add_u64 v[228:229], v[232:233], 0, s[20:21]
	s_mov_b32 m0, s6
	ds_read_b128 v[150:153], v161 offset:49152
	ds_read_b128 v[200:203], v161 offset:50176
	ds_read_b128 v[204:207], v161 offset:51200
	ds_read_b128 v[208:211], v161 offset:52224
	ds_read_b128 v[212:215], v161 offset:53248
	ds_read_b128 v[216:219], v161 offset:54272
	ds_read_b128 v[220:223], v161 offset:55296
	ds_read_b128 v[224:227], v161 offset:56320
	global_load_lds_dwordx4 v[228:229], off
	v_lshl_add_u64 v[228:229], v[234:235], 0, s[20:21]
	s_add_i32 m0, s6, 0x2000
	s_add_i32 s6, s31, s39
	global_load_lds_dwordx4 v[228:229], off
	v_lshl_add_u64 v[228:229], v[236:237], 0, s[20:21]
	s_mov_b32 m0, s6
	s_nop 0
	global_load_lds_dwordx4 v[228:229], off
	v_lshl_add_u64 v[228:229], v[238:239], 0, s[20:21]
	s_add_i32 m0, s6, 0x2000
	s_nop 0
	global_load_lds_dwordx4 v[228:229], off
	v_lshl_add_u64 v[228:229], v[240:241], 0, s[20:21]
	s_mov_b32 m0, s47
	s_nop 0
	global_load_lds_dwordx4 v[228:229], off
	v_lshl_add_u64 v[228:229], v[242:243], 0, s[20:21]
	s_mov_b32 m0, s48
	s_nop 0
	global_load_lds_dwordx4 v[228:229], off
	s_waitcnt vmcnt(8)
	s_waitcnt lgkmcnt(0)
	s_barrier
	s_waitcnt lgkmcnt(0)
	v_mfma_f32_16x16x32_bf16 v[60:63], v[166:169], v[150:153], v[60:63]
	v_mfma_f32_16x16x32_bf16 v[56:59], v[174:177], v[150:153], v[56:59]
	v_mfma_f32_16x16x32_bf16 v[44:47], v[166:169], v[204:207], v[44:47]
	v_mfma_f32_16x16x32_bf16 v[40:43], v[174:177], v[204:207], v[40:43]
	v_mfma_f32_16x16x32_bf16 v[28:31], v[166:169], v[212:215], v[28:31]
	v_mfma_f32_16x16x32_bf16 v[24:27], v[174:177], v[212:215], v[24:27]
	v_mfma_f32_16x16x32_bf16 v[12:15], v[166:169], v[220:223], v[12:15]
	v_mfma_f32_16x16x32_bf16 v[8:11], v[174:177], v[220:223], v[8:11]
	v_mfma_f32_16x16x32_bf16 v[60:63], v[170:173], v[200:203], v[60:63]
	v_mfma_f32_16x16x32_bf16 v[56:59], v[178:181], v[200:203], v[56:59]
	v_mfma_f32_16x16x32_bf16 v[44:47], v[170:173], v[208:211], v[44:47]
	v_mfma_f32_16x16x32_bf16 v[40:43], v[178:181], v[208:211], v[40:43]
	v_mfma_f32_16x16x32_bf16 v[28:31], v[170:173], v[216:219], v[28:31]
	v_mfma_f32_16x16x32_bf16 v[24:27], v[178:181], v[216:219], v[24:27]
	v_mfma_f32_16x16x32_bf16 v[12:15], v[170:173], v[224:227], v[12:15]
	v_mfma_f32_16x16x32_bf16 v[8:11], v[178:181], v[224:227], v[8:11]
	v_mfma_f32_16x16x32_bf16 v[52:55], v[182:185], v[150:153], v[52:55]
	v_mfma_f32_16x16x32_bf16 v[48:51], v[190:193], v[150:153], v[48:51]
	v_mfma_f32_16x16x32_bf16 v[36:39], v[182:185], v[204:207], v[36:39]
	v_mfma_f32_16x16x32_bf16 v[32:35], v[190:193], v[204:207], v[32:35]
	v_mfma_f32_16x16x32_bf16 v[20:23], v[182:185], v[212:215], v[20:23]
	v_mfma_f32_16x16x32_bf16 v[16:19], v[190:193], v[212:215], v[16:19]
	v_mfma_f32_16x16x32_bf16 v[4:7], v[182:185], v[220:223], v[4:7]
	v_mfma_f32_16x16x32_bf16 v[0:3], v[190:193], v[220:223], v[0:3]
	v_mfma_f32_16x16x32_bf16 v[52:55], v[186:189], v[200:203], v[52:55]
	v_mfma_f32_16x16x32_bf16 v[48:51], v[194:197], v[200:203], v[48:51]
	v_mfma_f32_16x16x32_bf16 v[36:39], v[186:189], v[208:211], v[36:39]
	v_mfma_f32_16x16x32_bf16 v[32:35], v[194:197], v[208:211], v[32:35]
	v_mfma_f32_16x16x32_bf16 v[20:23], v[186:189], v[216:219], v[20:23]
	v_mfma_f32_16x16x32_bf16 v[16:19], v[194:197], v[216:219], v[16:19]
	v_mfma_f32_16x16x32_bf16 v[4:7], v[186:189], v[224:227], v[4:7]
	v_mfma_f32_16x16x32_bf16 v[0:3], v[194:197], v[224:227], v[0:3]
	s_barrier
	s_add_i32 s61, s61, 2
	s_add_u32 s4, s4, 0x100
	s_addc_u32 s5, s5, 0
	s_cmp_gt_u32 s61, 13
	s_cbranch_scc1 .LBB0_842

.LBB0_1549:
	s_add_u32 s26, s4, s24
	s_addc_u32 s27, s5, s25
	s_add_u32 s28, s26, 0x28000100
	s_addc_u32 s29, s27, 0
	ds_read_b128 v[24:27], v252
	ds_read_b128 v[28:31], v253
	s_and_b64 s[26:27], s[30:31], exec
	ds_read_b128 v[16:19], v252 offset:2048
	ds_read_b128 v[20:23], v253 offset:2048
	s_cselect_b32 s27, s7, s29
	s_cselect_b32 s26, s6, s28
	s_add_u32 s63, s58, s24
	ds_read_b128 v[8:11], v252 offset:16384
	ds_read_b128 v[12:15], v253 offset:16384
	s_addc_u32 s64, s59, s25
	ds_read_b128 v[0:3], v252 offset:18432
	ds_read_b128 v[4:7], v253 offset:18432
	s_and_b64 s[28:29], s[30:31], exec
	s_cselect_b32 s29, s21, s64
	s_cselect_b32 s28, s20, s63
	s_add_u32 s63, s60, s24
	s_addc_u32 s64, s61, s25
	s_and_b64 s[30:31], s[30:31], exec
	s_cselect_b32 s31, s23, s64
	s_cselect_b32 s30, s22, s63
	s_add_u32 s100, s14, s24
	s_addc_u32 s101, s15, s25
	s_add_i32 m0, s35, 0xc000
	ds_read_b128 v[186:189], v206
	ds_read_b128 v[214:217], v206 offset:2048
	ds_read_b128 v[190:193], v207
	ds_read_b128 v[218:221], v207 offset:2048
	ds_read_b128 v[222:225], v206 offset:4096
	ds_read_b128 v[230:233], v206 offset:6144
	ds_read_b128 v[226:229], v207 offset:4096
	ds_read_b128 v[234:237], v207 offset:6144
	global_load_lds_dwordx4 v168, s[100:101]
	s_add_i32 m0, s35, 0xe000
	s_nop 0
	global_load_lds_dwordx4 v170, s[100:101]
	s_waitcnt vmcnt(8)
	s_waitcnt lgkmcnt(0)
	s_barrier
	s_waitcnt lgkmcnt(0)
	v_mfma_f32_16x16x128_f8f6f4 v[156:159], v[24:31], v[186:193], v[156:159]
	v_mfma_f32_16x16x128_f8f6f4 v[152:155], v[16:23], v[186:193], v[152:155]
	v_mfma_f32_16x16x128_f8f6f4 v[136:139], v[16:23], v[214:221], v[136:139]
	v_mfma_f32_16x16x128_f8f6f4 v[144:147], v[24:31], v[214:221], v[144:147]
	v_mfma_f32_16x16x128_f8f6f4 v[124:127], v[24:31], v[222:229], v[124:127]
	v_mfma_f32_16x16x128_f8f6f4 v[120:123], v[16:23], v[222:229], v[120:123]
	v_mfma_f32_16x16x128_f8f6f4 v[104:107], v[16:23], v[230:237], v[104:107]
	v_mfma_f32_16x16x128_f8f6f4 v[112:115], v[24:31], v[230:237], v[112:115]
	v_mfma_f32_16x16x128_f8f6f4 v[148:151], v[8:15], v[186:193], v[148:151]
	v_mfma_f32_16x16x128_f8f6f4 v[140:143], v[0:7], v[186:193], v[140:143]
	v_mfma_f32_16x16x128_f8f6f4 v[128:131], v[0:7], v[214:221], v[128:131]
	v_mfma_f32_16x16x128_f8f6f4 v[132:135], v[8:15], v[214:221], v[132:135]
	v_mfma_f32_16x16x128_f8f6f4 v[116:119], v[8:15], v[222:229], v[116:119]
	v_mfma_f32_16x16x128_f8f6f4 v[108:111], v[0:7], v[222:229], v[108:111]
	v_mfma_f32_16x16x128_f8f6f4 v[96:99], v[0:7], v[230:237], v[96:99]
	v_mfma_f32_16x16x128_f8f6f4 v[100:103], v[8:15], v[230:237], v[100:103]
	s_barrier
	s_add_i32 s63, s46, s34
	s_mov_b32 m0, s63
	ds_read_b128 v[214:217], v206 offset:16384
	ds_read_b128 v[222:225], v206 offset:18432
	ds_read_b128 v[218:221], v207 offset:16384
	ds_read_b128 v[226:229], v207 offset:18432
	ds_read_b128 v[230:233], v206 offset:20480
	ds_read_b128 v[238:241], v206 offset:22528
	ds_read_b128 v[234:237], v207 offset:20480
	ds_read_b128 v[242:245], v207 offset:22528
	global_load_lds_dwordx4 v160, s[28:29]
	s_add_i32 m0, s63, 0x2000
	s_add_i32 s98, s48, s34
	global_load_lds_dwordx4 v162, s[28:29]
	s_mov_b32 m0, s98
	s_nop 0
	global_load_lds_dwordx4 v160, s[30:31]
	s_add_i32 m0, s98, 0x2000
	v_mov_b32_e32 v167, v165
	global_load_lds_dwordx4 v162, s[30:31]
	s_waitcnt vmcnt(6)
	s_waitcnt lgkmcnt(0)
	s_barrier
	s_waitcnt lgkmcnt(0)
	v_mfma_f32_16x16x128_f8f6f4 v[92:95], v[24:31], v[214:221], v[92:95]
	v_mfma_f32_16x16x128_f8f6f4 v[88:91], v[16:23], v[214:221], v[88:91]
	v_mfma_f32_16x16x128_f8f6f4 v[72:75], v[16:23], v[222:229], v[72:75]
	v_mfma_f32_16x16x128_f8f6f4 v[80:83], v[24:31], v[222:229], v[80:83]
	s_mov_b32 m0, s35
	v_mfma_f32_16x16x128_f8f6f4 v[60:63], v[24:31], v[230:237], v[60:63]
	global_load_lds_dwordx4 v164, s[26:27]
	v_mfma_f32_16x16x128_f8f6f4 v[56:59], v[16:23], v[230:237], v[56:59]
	v_mfma_f32_16x16x128_f8f6f4 v[40:43], v[16:23], v[238:245], v[40:43]
	v_mfma_f32_16x16x128_f8f6f4 v[48:51], v[24:31], v[238:245], v[48:51]
	v_mfma_f32_16x16x128_f8f6f4 v[84:87], v[8:15], v[214:221], v[84:87]
	s_mov_b32 m0, s36
	v_mfma_f32_16x16x128_f8f6f4 v[76:79], v[0:7], v[214:221], v[76:79]
	global_load_lds_dwordx4 v166, s[26:27]
	v_mfma_f32_16x16x128_f8f6f4 v[64:67], v[0:7], v[222:229], v[64:67]
	v_mfma_f32_16x16x128_f8f6f4 v[68:71], v[8:15], v[222:229], v[68:71]
	v_mfma_f32_16x16x128_f8f6f4 v[52:55], v[8:15], v[230:237], v[52:55]
	v_mfma_f32_16x16x128_f8f6f4 v[44:47], v[0:7], v[230:237], v[44:47]
	v_mfma_f32_16x16x128_f8f6f4 v[32:35], v[0:7], v[238:245], v[32:35]
	v_mfma_f32_16x16x128_f8f6f4 v[36:39], v[8:15], v[238:245], v[36:39]
	s_barrier
	ds_read_b128 v[0:3], v252 offset:32768
	ds_read_b128 v[4:7], v253 offset:32768
	ds_read_b128 v[8:11], v252 offset:34816
	ds_read_b128 v[12:15], v253 offset:34816
	ds_read_b128 v[16:19], v252 offset:49152
	ds_read_b128 v[20:23], v253 offset:49152
	ds_read_b128 v[24:27], v252 offset:51200
	ds_read_b128 v[28:31], v253 offset:51200
	s_mov_b32 m0, s37
	ds_read_b128 v[214:217], v206 offset:32768
	ds_read_b128 v[222:225], v206 offset:34816
	ds_read_b128 v[218:221], v207 offset:32768
	ds_read_b128 v[226:229], v207 offset:34816
	ds_read_b128 v[230:233], v206 offset:36864
	ds_read_b128 v[238:241], v206 offset:38912
	ds_read_b128 v[234:237], v207 offset:36864
	ds_read_b128 v[242:245], v207 offset:38912
	global_load_lds_dwordx4 v184, s[26:27]
	s_mov_b32 m0, s38
	s_nop 0
	global_load_lds_dwordx4 v182, s[26:27]
	s_waitcnt vmcnt(8)
	s_waitcnt lgkmcnt(0)
	s_barrier
	s_waitcnt lgkmcnt(0)
	v_mfma_f32_16x16x128_f8f6f4 v[156:159], v[0:7], v[214:221], v[156:159]
	v_mfma_f32_16x16x128_f8f6f4 v[152:155], v[8:15], v[214:221], v[152:155]
	v_mfma_f32_16x16x128_f8f6f4 v[136:139], v[8:15], v[222:229], v[136:139]
	v_mfma_f32_16x16x128_f8f6f4 v[144:147], v[0:7], v[222:229], v[144:147]
	v_mfma_f32_16x16x128_f8f6f4 v[124:127], v[0:7], v[230:237], v[124:127]
	v_mfma_f32_16x16x128_f8f6f4 v[120:123], v[8:15], v[230:237], v[120:123]
	v_mfma_f32_16x16x128_f8f6f4 v[104:107], v[8:15], v[238:245], v[104:107]
	v_mfma_f32_16x16x128_f8f6f4 v[112:115], v[0:7], v[238:245], v[112:115]
	v_mfma_f32_16x16x128_f8f6f4 v[148:151], v[16:23], v[214:221], v[148:151]
	v_mfma_f32_16x16x128_f8f6f4 v[140:143], v[24:31], v[214:221], v[140:143]
	v_mfma_f32_16x16x128_f8f6f4 v[128:131], v[24:31], v[222:229], v[128:131]
	v_mfma_f32_16x16x128_f8f6f4 v[132:135], v[16:23], v[222:229], v[132:135]
	v_mfma_f32_16x16x128_f8f6f4 v[116:119], v[16:23], v[230:237], v[116:119]
	v_mfma_f32_16x16x128_f8f6f4 v[108:111], v[24:31], v[230:237], v[108:111]
	v_mfma_f32_16x16x128_f8f6f4 v[96:99], v[24:31], v[238:245], v[96:99]
	v_mfma_f32_16x16x128_f8f6f4 v[100:103], v[16:23], v[238:245], v[100:103]
	s_barrier
	s_add_i32 s99, s34, 0x17f80
	s_mov_b32 m0, s99
	ds_read_b128 v[214:217], v206 offset:49152
	ds_read_b128 v[222:225], v206 offset:51200
	ds_read_b128 v[218:221], v207 offset:49152
	ds_read_b128 v[226:229], v207 offset:51200
	ds_read_b128 v[230:233], v206 offset:53248
	ds_read_b128 v[238:241], v206 offset:55296
	ds_read_b128 v[234:237], v207 offset:53248
	ds_read_b128 v[242:245], v207 offset:55296
	global_load_lds_dwordx4 v160, s[28:29] offset:128
	s_add_i32 m0, s99, 0x2000
	s_add_i32 s99, s34, 0x1bf80
	global_load_lds_dwordx4 v162, s[28:29] offset:128
	s_mov_b32 m0, s99
	s_nop 0
	global_load_lds_dwordx4 v160, s[30:31] offset:128
	s_add_i32 m0, s99, 0x2000
	s_nop 0
	global_load_lds_dwordx4 v162, s[30:31] offset:128
	s_waitcnt vmcnt(6)
	s_waitcnt lgkmcnt(0)
	s_barrier
	s_waitcnt lgkmcnt(0)
	v_mfma_f32_16x16x128_f8f6f4 v[92:95], v[0:7], v[214:221], v[92:95]
	v_mfma_f32_16x16x128_f8f6f4 v[88:91], v[8:15], v[214:221], v[88:91]
	v_mfma_f32_16x16x128_f8f6f4 v[72:75], v[8:15], v[222:229], v[72:75]
	v_mfma_f32_16x16x128_f8f6f4 v[80:83], v[0:7], v[222:229], v[80:83]
	s_add_i32 m0, s41, 0xffffff80
	v_mfma_f32_16x16x128_f8f6f4 v[60:63], v[0:7], v[230:237], v[60:63]
	global_load_lds_dwordx4 v164, s[26:27] offset:128
	v_mfma_f32_16x16x128_f8f6f4 v[56:59], v[8:15], v[230:237], v[56:59]
	v_mfma_f32_16x16x128_f8f6f4 v[40:43], v[8:15], v[238:245], v[40:43]
	v_mfma_f32_16x16x128_f8f6f4 v[48:51], v[0:7], v[238:245], v[48:51]
	v_mfma_f32_16x16x128_f8f6f4 v[84:87], v[16:23], v[214:221], v[84:87]
	s_add_i32 m0, s42, 0xffffff80
	v_mfma_f32_16x16x128_f8f6f4 v[76:79], v[24:31], v[214:221], v[76:79]
	global_load_lds_dwordx4 v166, s[26:27] offset:128
	v_mfma_f32_16x16x128_f8f6f4 v[64:67], v[24:31], v[222:229], v[64:67]
	v_mfma_f32_16x16x128_f8f6f4 v[68:71], v[16:23], v[222:229], v[68:71]
	v_mfma_f32_16x16x128_f8f6f4 v[52:55], v[16:23], v[230:237], v[52:55]
	v_mfma_f32_16x16x128_f8f6f4 v[44:47], v[24:31], v[230:237], v[44:47]
	v_mfma_f32_16x16x128_f8f6f4 v[32:35], v[24:31], v[238:245], v[32:35]
	v_mfma_f32_16x16x128_f8f6f4 v[36:39], v[16:23], v[238:245], v[36:39]
	s_barrier
	s_add_i32 s62, s62, 2
	s_add_u32 s24, s24, 0x100
	s_addc_u32 s25, s25, 0
	s_cmp_gt_u32 s62, 29
	s_cbranch_scc1 .LBB0_1552
